# v35 + code placement: 13 hot loop headers (7 GEMM K-loops, MLA/DA/NA tile loops, PU, PTK, rtp) aligned to 64-byte boundaries with .p2align 6
# speedup vs baseline: 1.0008x; 1.0007x over previous
.LBB0_350:
	v_mov_b64_e32 v[0:1], 0x6c0
	v_cmp_lt_i64_e32 vcc, s[6:7], v[0:1]
	s_lshl_b32 s34, s31, 19
	s_and_b64 s[6:7], vcc, exec
	s_cselect_b32 s6, s34, s10
	s_lshl_b32 s35, s30, 19
	s_and_b64 s[40:41], vcc, exec
	v_mov_b32_e32 v0, 0
	v_mov_b32_e32 v213, 0x3ba10414
	v_mov_b32_e32 v252, 2
	s_cselect_b32 s7, s35, s39
	s_add_i32 s38, s10, 0x40080
	s_addk_i32 s39, 0x100
	s_mov_b32 s40, -2
	v_mov_b32_e32 v1, v0
	v_mov_b32_e32 v2, v0
	v_mov_b32_e32 v3, v0
	v_mov_b32_e32 v4, v0
	v_mov_b32_e32 v5, v0
	v_mov_b32_e32 v6, v0
	v_mov_b32_e32 v7, v0
	v_mov_b32_e32 v8, v0
	v_mov_b32_e32 v9, v0
	v_mov_b32_e32 v10, v0
	v_mov_b32_e32 v11, v0
	v_mov_b32_e32 v208, v0
	v_mov_b32_e32 v209, v0
	v_mov_b32_e32 v210, v0
	v_mov_b32_e32 v211, v0
	v_mov_b32_e32 v24, v0
	v_mov_b32_e32 v25, v0
	v_mov_b32_e32 v26, v0
	v_mov_b32_e32 v27, v0
	v_mov_b32_e32 v32, v0
	v_mov_b32_e32 v33, v0
	v_mov_b32_e32 v34, v0
	v_mov_b32_e32 v35, v0
	v_mov_b32_e32 v40, v0
	v_mov_b32_e32 v41, v0
	v_mov_b32_e32 v42, v0
	v_mov_b32_e32 v43, v0
	v_mov_b32_e32 v48, v0
	v_mov_b32_e32 v49, v0
	v_mov_b32_e32 v50, v0
	v_mov_b32_e32 v51, v0
	v_mov_b32_e32 v12, v0
	v_mov_b32_e32 v13, v0
	v_mov_b32_e32 v14, v0
	v_mov_b32_e32 v15, v0
	v_mov_b32_e32 v20, v0
	v_mov_b32_e32 v21, v0
	v_mov_b32_e32 v22, v0
	v_mov_b32_e32 v23, v0
	v_mov_b32_e32 v28, v0
	v_mov_b32_e32 v29, v0
	v_mov_b32_e32 v30, v0
	v_mov_b32_e32 v31, v0
	v_mov_b32_e32 v36, v0
	v_mov_b32_e32 v37, v0
	v_mov_b32_e32 v38, v0
	v_mov_b32_e32 v39, v0
	v_mov_b32_e32 v44, v0
	v_mov_b32_e32 v45, v0
	v_mov_b32_e32 v46, v0
	v_mov_b32_e32 v47, v0
	v_mov_b32_e32 v52, v0
	v_mov_b32_e32 v53, v0
	v_mov_b32_e32 v54, v0
	v_mov_b32_e32 v55, v0
	v_mov_b32_e32 v56, v0
	v_mov_b32_e32 v57, v0
	v_mov_b32_e32 v58, v0
	v_mov_b32_e32 v59, v0
	v_mov_b32_e32 v60, v0
	v_mov_b32_e32 v61, v0
	v_mov_b32_e32 v62, v0
	v_mov_b32_e32 v63, v0
	v_mov_b32_e32 v16, v0
	v_mov_b32_e32 v17, v0
	v_mov_b32_e32 v18, v0
	v_mov_b32_e32 v19, v0
	v_mov_b32_e32 v68, v0
	v_mov_b32_e32 v69, v0
	v_mov_b32_e32 v70, v0
	v_mov_b32_e32 v71, v0
	v_mov_b32_e32 v72, v0
	v_mov_b32_e32 v73, v0
	v_mov_b32_e32 v74, v0
	v_mov_b32_e32 v75, v0
	v_mov_b32_e32 v76, v0
	v_mov_b32_e32 v77, v0
	v_mov_b32_e32 v78, v0
	v_mov_b32_e32 v79, v0
	v_mov_b32_e32 v88, v0
	v_mov_b32_e32 v89, v0
	v_mov_b32_e32 v90, v0
	v_mov_b32_e32 v91, v0
	v_mov_b32_e32 v92, v0
	v_mov_b32_e32 v93, v0
	v_mov_b32_e32 v94, v0
	v_mov_b32_e32 v95, v0
	v_mov_b32_e32 v106, v0
	v_mov_b32_e32 v107, v0
	v_mov_b32_e32 v108, v0
	v_mov_b32_e32 v109, v0
	v_mov_b32_e32 v110, v0
	v_mov_b32_e32 v111, v0
	v_mov_b32_e32 v112, v0
	v_mov_b32_e32 v113, v0
	v_mov_b32_e32 v80, v0
	v_mov_b32_e32 v81, v0
	v_mov_b32_e32 v82, v0
	v_mov_b32_e32 v83, v0
	v_mov_b32_e32 v84, v0
	v_mov_b32_e32 v85, v0
	v_mov_b32_e32 v86, v0
	v_mov_b32_e32 v87, v0
	v_mov_b32_e32 v98, v0
	v_mov_b32_e32 v99, v0
	v_mov_b32_e32 v100, v0
	v_mov_b32_e32 v101, v0
	v_mov_b32_e32 v102, v0
	v_mov_b32_e32 v103, v0
	v_mov_b32_e32 v104, v0
	v_mov_b32_e32 v105, v0
	v_mov_b32_e32 v114, v0
	v_mov_b32_e32 v115, v0
	v_mov_b32_e32 v116, v0
	v_mov_b32_e32 v117, v0
	v_mov_b32_e32 v118, v0
	v_mov_b32_e32 v119, v0
	v_mov_b32_e32 v120, v0
	v_mov_b32_e32 v121, v0
	v_mov_b32_e32 v122, v0
	v_mov_b32_e32 v123, v0
	v_mov_b32_e32 v124, v0
	v_mov_b32_e32 v125, v0
	v_mov_b32_e32 v126, v0
	v_mov_b32_e32 v127, v0
	v_mov_b32_e32 v128, v0
	v_mov_b32_e32 v129, v0
	.p2align 6

.LBB0_483:
	v_mov_b64_e32 v[0:1], 0xd8
	v_cmp_lt_i64_e32 vcc, s[6:7], v[0:1]
	s_mul_i32 s38, s37, 0x300000
	s_and_b64 s[6:7], vcc, exec
	s_cselect_b32 s6, s38, s11
	s_lshl_b32 s39, s36, 18
	s_and_b64 s[42:43], vcc, exec
	v_mov_b32_e32 v0, 0
	s_cselect_b32 s7, s39, s10
	s_add_i32 s42, s11, 0x180080
	s_add_i32 s43, s10, 0x100
	s_mov_b32 s44, -2
	v_mov_b32_e32 v1, v0
	v_mov_b32_e32 v2, v0
	v_mov_b32_e32 v3, v0
	v_mov_b32_e32 v4, v0
	v_mov_b32_e32 v5, v0
	v_mov_b32_e32 v6, v0
	v_mov_b32_e32 v7, v0
	v_mov_b32_e32 v8, v0
	v_mov_b32_e32 v9, v0
	v_mov_b32_e32 v10, v0
	v_mov_b32_e32 v11, v0
	v_mov_b32_e32 v12, v0
	v_mov_b32_e32 v13, v0
	v_mov_b32_e32 v14, v0
	v_mov_b32_e32 v15, v0
	v_mov_b32_e32 v24, v0
	v_mov_b32_e32 v25, v0
	v_mov_b32_e32 v26, v0
	v_mov_b32_e32 v27, v0
	v_mov_b32_e32 v28, v0
	v_mov_b32_e32 v29, v0
	v_mov_b32_e32 v30, v0
	v_mov_b32_e32 v31, v0
	v_mov_b32_e32 v40, v0
	v_mov_b32_e32 v41, v0
	v_mov_b32_e32 v42, v0
	v_mov_b32_e32 v43, v0
	v_mov_b32_e32 v44, v0
	v_mov_b32_e32 v45, v0
	v_mov_b32_e32 v46, v0
	v_mov_b32_e32 v47, v0
	v_mov_b32_e32 v16, v0
	v_mov_b32_e32 v17, v0
	v_mov_b32_e32 v18, v0
	v_mov_b32_e32 v19, v0
	v_mov_b32_e32 v20, v0
	v_mov_b32_e32 v21, v0
	v_mov_b32_e32 v22, v0
	v_mov_b32_e32 v23, v0
	v_mov_b32_e32 v32, v0
	v_mov_b32_e32 v33, v0
	v_mov_b32_e32 v34, v0
	v_mov_b32_e32 v35, v0
	v_mov_b32_e32 v36, v0
	v_mov_b32_e32 v37, v0
	v_mov_b32_e32 v38, v0
	v_mov_b32_e32 v39, v0
	v_mov_b32_e32 v48, v0
	v_mov_b32_e32 v49, v0
	v_mov_b32_e32 v50, v0
	v_mov_b32_e32 v51, v0
	v_mov_b32_e32 v52, v0
	v_mov_b32_e32 v53, v0
	v_mov_b32_e32 v54, v0
	v_mov_b32_e32 v55, v0
	v_mov_b32_e32 v56, v0
	v_mov_b32_e32 v57, v0
	v_mov_b32_e32 v58, v0
	v_mov_b32_e32 v59, v0
	v_mov_b32_e32 v60, v0
	v_mov_b32_e32 v61, v0
	v_mov_b32_e32 v62, v0
	v_mov_b32_e32 v63, v0
	v_mov_b32_e32 v64, v0
	v_mov_b32_e32 v65, v0
	v_mov_b32_e32 v66, v0
	v_mov_b32_e32 v67, v0
	v_mov_b32_e32 v68, v0
	v_mov_b32_e32 v69, v0
	v_mov_b32_e32 v70, v0
	v_mov_b32_e32 v71, v0
	v_mov_b32_e32 v72, v0
	v_mov_b32_e32 v73, v0
	v_mov_b32_e32 v74, v0
	v_mov_b32_e32 v75, v0
	v_mov_b32_e32 v76, v0
	v_mov_b32_e32 v77, v0
	v_mov_b32_e32 v78, v0
	v_mov_b32_e32 v79, v0
	v_mov_b32_e32 v88, v0
	v_mov_b32_e32 v89, v0
	v_mov_b32_e32 v90, v0
	v_mov_b32_e32 v91, v0
	v_mov_b32_e32 v92, v0
	v_mov_b32_e32 v93, v0
	v_mov_b32_e32 v94, v0
	v_mov_b32_e32 v95, v0
	v_mov_b32_e32 v106, v0
	v_mov_b32_e32 v107, v0
	v_mov_b32_e32 v108, v0
	v_mov_b32_e32 v109, v0
	v_mov_b32_e32 v110, v0
	v_mov_b32_e32 v111, v0
	v_mov_b32_e32 v112, v0
	v_mov_b32_e32 v113, v0
	v_mov_b32_e32 v80, v0
	v_mov_b32_e32 v81, v0
	v_mov_b32_e32 v82, v0
	v_mov_b32_e32 v83, v0
	v_mov_b32_e32 v84, v0
	v_mov_b32_e32 v85, v0
	v_mov_b32_e32 v86, v0
	v_mov_b32_e32 v87, v0
	v_mov_b32_e32 v98, v0
	v_mov_b32_e32 v99, v0
	v_mov_b32_e32 v100, v0
	v_mov_b32_e32 v101, v0
	v_mov_b32_e32 v102, v0
	v_mov_b32_e32 v103, v0
	v_mov_b32_e32 v104, v0
	v_mov_b32_e32 v105, v0
	v_mov_b32_e32 v114, v0
	v_mov_b32_e32 v115, v0
	v_mov_b32_e32 v116, v0
	v_mov_b32_e32 v117, v0
	v_mov_b32_e32 v118, v0
	v_mov_b32_e32 v119, v0
	v_mov_b32_e32 v120, v0
	v_mov_b32_e32 v121, v0
	v_mov_b32_e32 v122, v0
	v_mov_b32_e32 v123, v0
	v_mov_b32_e32 v124, v0
	v_mov_b32_e32 v125, v0
	v_mov_b32_e32 v126, v0
	v_mov_b32_e32 v127, v0
	v_mov_b32_e32 v128, v0
	v_mov_b32_e32 v129, v0
	.p2align 6

.LBB0_593:
	s_or_b64 exec, exec, s[20:21]
	s_getreg_b32 s0, hwreg(HW_REG_HW_ID, 0, 6)
	s_and_b32 s0, s0, 63
	s_lshl_b32 s0, s0, 2
	s_add_i32 s0, s0, 0
	s_add_i32 s0, s0, 0x20010
	v_mov_b32_e32 v0, s0
	ds_read_b32 v0, v0
	v_readlane_b32 s4, v254, 26
	s_mov_b32 s2, 0x40000
	v_readlane_b32 s5, v254, 27
	s_waitcnt lgkmcnt(0)
	v_readfirstlane_b32 s0, v0
	v_mbcnt_lo_u32_b32 v0, -1, 0
	v_mbcnt_hi_u32_b32 v0, -1, v0
	s_nop 1
	v_lshl_or_b32 v0, s0, 6, v0
	v_add_u32_e32 v1, s4, v0
	v_cmp_gt_i32_e32 vcc, s2, v1
	s_and_saveexec_b64 s[4:5], vcc
	v_readlane_b32 s14, v254, 43
	v_readlane_b32 s15, v254, 44
	s_mov_b32 s15, 0x10000
	v_readlane_b32 s16, v254, 22
	s_mov_b32 s17, 0x8000
	s_mov_b32 s20, 0x30000
	s_mov_b32 s21, 0x60000
	s_mov_b32 s22, 0x90000
	s_mov_b32 s23, 0x50000
	s_mov_b32 s24, 0x28000
	s_mov_b32 s25, 0x70000
	s_mov_b32 s26, 0x80000
	s_mov_b32 s27, 0xa0000
	s_mov_b32 s28, 0xb0000
	s_mov_b32 s29, 0x100000
	s_cbranch_execz .LBB0_596
	s_add_u32 s6, s18, 0xe2000
	s_addc_u32 s7, s19, 0
	s_add_u32 s8, s18, 0x21b00000
	s_addc_u32 s9, s19, 0
	s_add_u32 s10, s18, 0x26300000
	v_readlane_b32 s0, v254, 21
	s_addc_u32 s11, s19, 0
	s_mov_b64 s[12:13], 0
	v_lshl_add_u32 v6, v0, 2, s0
	.p2align 6

.LBB0_651:
	s_and_b32 s2, s18, 7
	s_bfe_u32 s20, s19, 0x20003
	s_mul_i32 s4, s2, 0x60000
	s_mul_i32 s0, s20, 0x180
	s_or_b32 s4, s4, s0
	s_add_u32 s8, s14, s4
	s_addc_u32 s9, s15, 0
	s_lshl_b32 s2, s2, 19
	s_lshl_b32 s12, s20, 9
	s_or_b32 s2, s2, s12
	s_add_u32 s10, s16, s2
	s_getreg_b32 s2, hwreg(HW_REG_HW_ID, 0, 6)
	s_addc_u32 s11, s17, 0
	s_and_b32 s2, s2, 63
	s_lshl_b32 s2, s2, 2
	s_add_i32 s2, s2, 0
	s_add_i32 s2, s2, 0x20010
	v_mov_b32_e32 v0, s2
	ds_read_b32 v0, v0
	s_and_b32 s13, s19, 7
	s_lshl_b32 s4, s19, 3
	s_lshl_b32 s2, s13, 11
	s_and_b32 s4, s4, 0xffffff00
	s_add_i32 s2, s2, s4
	s_waitcnt lgkmcnt(0)
	v_readfirstlane_b32 s4, v0
	s_lshl_b32 s24, s4, 6
	s_waitcnt vmcnt(1)
	v_mbcnt_lo_u32_b32 v23, -1, 0
	v_mbcnt_hi_u32_b32 v23, -1, v23
	v_readlane_b32 s4, v255, 5
	s_waitcnt vmcnt(0)
	v_or_b32_e32 v18, s24, v23
	v_ashrrev_i32_e32 v0, 1, v18
	v_and_b32_e32 v0, 0xffffffe0, v0
	v_and_b32_e32 v189, 31, v23
	v_add_u32_e32 v168, s2, v0
	v_readlane_b32 s5, v255, 6
	v_or_b32_e32 v2, v168, v189
	s_movk_i32 s25, 0x600
	v_mov_b64_e32 v[0:1], s[4:5]
	s_lshl_b32 s2, s13, 8
	v_mad_i64_i32 v[0:1], s[4:5], v2, s25, v[0:1]
	s_bitset1_b32 s2, 14
	s_mul_i32 s4, s2, 0x600
	v_readlane_b32 s21, v255, 7
	s_add_u32 s4, s21, s4
	v_readlane_b32 s22, v255, 8
	s_addc_u32 s5, s22, 0
	s_add_u32 s4, s4, s0
	s_addc_u32 s5, s5, 0
	s_lshl_b32 s2, s2, 11
	v_readlane_b32 s23, v255, 9
	s_add_u32 s2, s23, s2
	v_readlane_b32 s26, v255, 10
	s_addc_u32 s7, s26, 0
	v_lshlrev_b32_e32 v28, 3, v23
	v_add_u32_e32 v12, 0x200, v18
	v_bfe_u32 v188, v23, 5, 1
	s_add_u32 s6, s2, s12
	v_and_b32_e32 v22, 0x78, v28
	v_ashrrev_i32_e32 v24, 4, v18
	v_ashrrev_i32_e32 v26, 4, v12
	v_lshl_add_u64 v[0:1], v[0:1], 0, s[0:1]
	v_lshlrev_b32_e32 v170, 4, v188
	v_mov_b32_e32 v171, v97
	s_addc_u32 s7, s7, 0
	v_lshlrev_b32_e32 v96, 1, v22
	v_ashrrev_i32_e32 v25, 31, v24
	v_ashrrev_i32_e32 v27, 31, v26
	v_lshl_add_u64 v[20:21], v[0:1], 0, v[170:171]
	v_lshl_add_u64 v[0:1], s[6:7], 0, v[96:97]
	v_lshlrev_b64 v[172:173], 11, v[24:25]
	v_lshlrev_b64 v[174:175], 11, v[26:27]
	v_lshl_add_u64 v[2:3], v[0:1], 0, v[172:173]
	v_lshl_add_u64 v[4:5], v[0:1], 0, v[174:175]
	s_mov_b32 s2, 0x2aaaaaab
	global_load_dwordx4 v[102:105], v[20:21], off
	global_load_dwordx4 v[98:101], v[20:21], off offset:32
	s_nop 0
	global_load_dwordx4 v[0:3], v[2:3], off offset:256
	s_nop 0
	global_load_dwordx4 v[4:7], v[4:5], off offset:256
	v_mul_hi_i32 v8, v18, s2
	v_lshrrev_b32_e32 v9, 31, v8
	v_ashrrev_i32_e32 v8, 2, v8
	v_add_u32_e32 v25, v8, v9
	v_mul_lo_u32 v10, v25, 24
	v_sub_u32_e32 v27, v18, v10
	v_mul_hi_i32 v10, v12, s2
	v_lshrrev_b32_e32 v11, 31, v10
	v_ashrrev_i32_e32 v10, 2, v10
	v_add_u32_e32 v29, v10, v11
	v_mul_lo_u32 v13, v29, 24
	v_sub_u32_e32 v30, v12, v13
	v_mov_b64_e32 v[16:17], s[4:5]
	v_lshlrev_b32_e32 v176, 3, v27
	v_lshlrev_b32_e32 v178, 3, v30
	v_mad_i64_i32 v[8:9], s[4:5], v25, s25, v[16:17]
	v_ashrrev_i32_e32 v177, 31, v176
	v_mad_i64_i32 v[10:11], s[4:5], v29, s25, v[16:17]
	v_ashrrev_i32_e32 v179, 31, v178
	v_lshl_add_u64 v[8:9], v[176:177], 1, v[8:9]
	v_lshl_add_u64 v[12:13], v[178:179], 1, v[10:11]
	global_load_dwordx4 v[8:11], v[8:9], off
	s_nop 0
	global_load_dwordx4 v[12:15], v[12:13], off
	v_add_u32_e32 v18, 0x400, v18
	v_mul_hi_i32 v19, v18, s2
	v_lshrrev_b32_e32 v31, 31, v19
	v_ashrrev_i32_e32 v19, 2, v19
	v_add_u32_e32 v31, v19, v31
	v_mul_lo_u32 v19, v31, 24
	v_sub_u32_e32 v32, v18, v19
	v_lshlrev_b32_e32 v180, 3, v32
	v_mad_i64_i32 v[16:17], s[4:5], v31, s25, v[16:17]
	v_ashrrev_i32_e32 v181, 31, v180
	v_lshl_add_u64 v[16:17], v[180:181], 1, v[16:17]
	global_load_dwordx4 v[16:19], v[16:17], off
	s_nop 0
	global_load_dwordx4 v[142:145], v[20:21], off offset:64
	global_load_dwordx4 v[138:141], v[20:21], off offset:96
	global_load_dwordx4 v[134:137], v[20:21], off offset:128
	global_load_dwordx4 v[130:133], v[20:21], off offset:160
	global_load_dwordx4 v[126:129], v[20:21], off offset:192
	global_load_dwordx4 v[122:125], v[20:21], off offset:224
	global_load_dwordx4 v[118:121], v[20:21], off offset:256
	global_load_dwordx4 v[114:117], v[20:21], off offset:288
	global_load_dwordx4 v[110:113], v[20:21], off offset:320
	global_load_dwordx4 v[106:109], v[20:21], off offset:352
	v_lshlrev_b32_e32 v21, 4, v23
	v_and_b32_e32 v34, 0xc0, v21
	v_and_b32_e32 v198, 48, v21
	v_and_b32_e32 v21, 0xfffff0, v24
	v_lshlrev_b32_e32 v36, 1, v24
	v_and_or_b32 v21, v36, 8, v21
	v_bfe_u32 v35, v28, 5, 2
	v_lshrrev_b32_e32 v21, 1, v21
	v_or_b32_e32 v21, v21, v35
	v_lshrrev_b32_e32 v36, 1, v24
	v_lshlrev_b32_e32 v200, 9, v21
	v_and_b32_e32 v21, 3, v24
	v_and_or_b32 v21, v36, 4, v21
	v_lshlrev_b32_e32 v202, 6, v21
	v_add_u32_e32 v21, 0, v200
	v_add3_u32 v21, v21, v202, v198
	s_mul_i32 s2, s13, 0x300000
	s_waitcnt vmcnt(0)
	s_add_u32 s2, s21, s2
	s_addc_u32 s4, s22, 0
	s_add_u32 s2, s2, s0
	s_addc_u32 s21, s4, 0
	s_lshl_b32 s0, s13, 22
	s_add_u32 s0, s23, s0
	s_addc_u32 s4, s26, 0
	s_add_u32 s22, s0, s12
	v_mov_b32_e32 v20, 0x3fffffc0
	s_addc_u32 s23, s4, 0
	v_bitop3_b32 v20, s24, v20, v23 bitop3:0xc8
	s_add_i32 s0, 0, 0x14000
	v_lshl_add_u32 v171, v20, 2, s0
	s_movk_i32 s0, 0x180
	v_mul_lo_u32 v207, v25, s0
	v_mul_lo_u32 v229, v29, s0
	v_mul_lo_u32 v231, v31, s0
	v_lshlrev_b32_e32 v33, 1, v23
	s_cmp_lg_u32 0, -1
	v_and_b32_e32 v20, 63, v23
	v_mad_i64_i32 v[182:183], s[4:5], v25, s25, 0
	v_mad_i64_i32 v[184:185], s[4:5], v29, s25, 0
	s_waitcnt vmcnt(14)
	ds_write_b128 v21, v[0:3]
	v_and_b32_e32 v0, 0xfffff0, v26
	v_lshlrev_b32_e32 v1, 1, v26
	v_and_or_b32 v0, v1, 8, v0
	v_lshrrev_b32_e32 v0, 1, v0
	v_or_b32_e32 v0, v0, v35
	v_lshrrev_b32_e32 v1, 1, v26
	v_lshlrev_b32_e32 v204, 9, v0
	v_and_b32_e32 v0, 3, v26
	v_and_or_b32 v0, v1, 4, v0
	v_lshlrev_b32_e32 v205, 6, v0
	v_add_u32_e32 v0, 0, v204
	v_add3_u32 v0, v0, v205, v198
	s_waitcnt vmcnt(13)
	ds_write_b128 v0, v[4:7]
	v_lshrrev_b32_e32 v0, 1, v25
	v_bitop3_b32 v0, v0, v27, 7 bitop3:0x6c
	v_lshlrev_b32_e32 v227, 4, v0
	v_add3_u32 v0, 0, v227, v207
	v_bfe_u32 v1, v23, 1, 3
	v_mad_i64_i32 v[186:187], s[4:5], v31, s25, 0
	s_cselect_b32 s0, 0, 0
	v_cmp_gt_u32_e64 s[4:5], 32, v20
	s_waitcnt vmcnt(12)
	ds_write_b128 v0, v[8:11] offset:32768
	v_lshrrev_b32_e32 v0, 1, v29
	v_bitop3_b32 v0, v0, v30, 7 bitop3:0x6c
	v_lshlrev_b32_e32 v230, 4, v0
	v_add3_u32 v0, 0, v230, v229
	s_waitcnt vmcnt(11)
	ds_write_b128 v0, v[12:15] offset:32768
	v_lshrrev_b32_e32 v0, 1, v31
	v_bitop3_b32 v0, v0, v32, 7 bitop3:0x6c
	v_lshlrev_b32_e32 v233, 4, v0
	v_add3_u32 v0, 0, v233, v231
	s_waitcnt vmcnt(10)
	ds_write_b128 v0, v[16:19] offset:32768
	v_lshrrev_b32_e32 v0, 1, v23
	v_bitop3_b32 v0, v188, v0, 7 bitop3:0x78
	v_lshlrev_b32_e32 v235, 4, v0
	v_bitop3_b32 v0, v188, v1, 2 bitop3:0x36
	v_lshlrev_b32_e32 v232, 4, v0
	v_bitop3_b32 v0, v188, v1, 4 bitop3:0x36
	v_lshlrev_b32_e32 v228, 4, v0
	v_bitop3_b32 v0, v188, v1, 6 bitop3:0x36
	v_lshlrev_b32_e32 v206, 4, v0
	v_bitop3_b32 v0, v188, v1, 8 bitop3:0x36
	v_lshlrev_b32_e32 v203, 4, v0
	v_bitop3_b32 v0, v188, v1, 10 bitop3:0x36
	v_lshlrev_b32_e32 v201, 4, v0
	v_bitop3_b32 v0, v188, v1, 12 bitop3:0x36
	v_lshlrev_b32_e32 v199, 4, v0
	v_bitop3_b32 v0, v188, v1, 14 bitop3:0x36
	v_lshlrev_b32_e32 v196, 4, v0
	v_bitop3_b32 v0, v188, v1, 16 bitop3:0x36
	v_lshlrev_b32_e32 v195, 4, v0
	v_bitop3_b32 v0, v188, v1, 18 bitop3:0x36
	v_lshlrev_b32_e32 v194, 4, v0
	v_bitop3_b32 v0, v188, v1, 20 bitop3:0x36
	v_lshlrev_b32_e32 v193, 4, v0
	v_bitop3_b32 v0, v188, v1, 22 bitop3:0x36
	v_lshlrev_b32_e32 v192, 4, v0
	v_and_b32_e32 v0, 0x118, v28
	v_and_or_b32 v0, v33, 32, v0
	v_mov_b32_e32 v14, v97
	v_mov_b32_e32 v15, v97
	v_add3_u32 v190, v34, s0, v0
	v_mov_b32_e32 v0, v97
	v_mov_b32_e32 v1, v97
	v_mov_b32_e32 v2, v97
	v_mov_b32_e32 v3, v97
	v_mov_b32_e32 v4, v97
	v_mov_b32_e32 v5, v97
	v_mov_b32_e32 v6, v97
	v_mov_b32_e32 v7, v97
	v_mov_b32_e32 v8, v97
	v_mov_b32_e32 v9, v97
	v_mov_b32_e32 v10, v97
	v_mov_b32_e32 v11, v97
	v_mov_b32_e32 v12, v97
	v_mov_b32_e32 v13, v97
	v_lshlrev_b32_e32 v96, 1, v22
	v_mov_b64_e32 v[30:31], v[14:15]
	v_mov_b64_e32 v[46:47], v[14:15]
	v_mov_b64_e32 v[62:63], v[14:15]
	v_mul_u32_u24_e32 v234, 0x180, v189
	v_lshl_add_u32 v169, v189, 2, v171
	v_mov_b32_e32 v191, 0xf149f2ca
	v_mov_b32_e32 v236, 0
	s_mov_b32 s0, -3
	v_mov_b64_e32 v[28:29], v[12:13]
	v_mov_b64_e32 v[26:27], v[10:11]
	v_mov_b64_e32 v[24:25], v[8:9]
	v_mov_b64_e32 v[22:23], v[6:7]
	v_mov_b64_e32 v[20:21], v[4:5]
	v_mov_b64_e32 v[18:19], v[2:3]
	v_mov_b64_e32 v[16:17], v[0:1]
	v_mov_b64_e32 v[44:45], v[12:13]
	v_mov_b64_e32 v[42:43], v[10:11]
	v_mov_b64_e32 v[40:41], v[8:9]
	v_mov_b64_e32 v[38:39], v[6:7]
	v_mov_b64_e32 v[36:37], v[4:5]
	v_mov_b64_e32 v[34:35], v[2:3]
	v_mov_b64_e32 v[32:33], v[0:1]
	v_mov_b64_e32 v[60:61], v[12:13]
	v_mov_b64_e32 v[58:59], v[10:11]
	v_mov_b64_e32 v[56:57], v[8:9]
	v_mov_b64_e32 v[54:55], v[6:7]
	v_mov_b64_e32 v[52:53], v[4:5]
	v_mov_b64_e32 v[50:51], v[2:3]
	v_mov_b64_e32 v[48:49], v[0:1]
	s_waitcnt lgkmcnt(0)
	s_barrier
	.p2align 6

.LBB0_671:
	s_lshl_b32 s0, s35, 1
	s_and_b32 s2, s34, 7
	s_and_b32 s0, s0, 0x300
	s_mul_i32 s4, s2, 0x300000
	s_add_u32 s39, s96, s4
	s_getreg_b32 s4, hwreg(HW_REG_HW_ID, 0, 6)
	s_addc_u32 s40, s97, 0
	s_and_b32 s4, s4, 63
	s_lshl_b32 s4, s4, 2
	s_add_i32 s4, s4, 0
	s_add_i32 s4, s4, 0x20010
	v_mov_b32_e32 v0, s4
	ds_read_b32 v0, v0
	s_and_b32 s8, s36, 7
	s_lshl_b32 s4, s36, 2
	s_lshl_b32 s37, s8, 11
	s_and_b32 s4, s4, 0xffffff80
	s_add_i32 s37, s37, s4
	s_waitcnt lgkmcnt(0)
	v_readfirstlane_b32 s4, v0
	s_lshl_b32 s9, s4, 6
	s_lshl_b32 s4, s36, 4
	s_and_b32 s38, s4, 0x180
	s_lshl_b32 s6, s38, 1
	s_mul_i32 s4, s8, 0x300000
	s_add_u32 s4, s84, s4
	s_waitcnt vmcnt(2)
	v_mbcnt_lo_u32_b32 v49, -1, 0
	v_mbcnt_hi_u32_b32 v49, -1, v49
	s_addc_u32 s5, s85, 0
	s_waitcnt vmcnt(1)
	v_lshlrev_b32_e32 v20, 3, v49
	s_add_u32 s4, s4, s6
	v_and_b32_e32 v48, 0x78, v20
	v_or_b32_e32 v187, s9, v49
	s_addc_u32 s5, s5, 0
	v_lshlrev_b32_e32 v0, 1, v48
	v_mov_b32_e32 v1, v97
	v_lshl_add_u64 v[54:55], s[4:5], 0, v[0:1]
	s_mov_b64 s[12:13], 0xc000800
	v_add_u32_e32 v14, 0x200, v187
	v_lshl_add_u64 v[0:1], v[54:55], 0, s[12:13]
	v_ashrrev_i32_e32 v76, 4, v187
	v_ashrrev_i32_e32 v77, 4, v14
	v_mad_i64_i32 v[2:3], s[12:13], v76, s95, v[0:1]
	v_mad_i64_i32 v[4:5], s[12:13], v77, s95, v[0:1]
	v_ashrrev_i32_e32 v8, 31, v187
	global_load_dwordx4 v[0:3], v[2:3], off
	s_nop 0
	global_load_dwordx4 v[4:7], v[4:5], off
	v_lshrrev_b32_e32 v8, 28, v8
	v_add_u32_e32 v10, v187, v8
	v_ashrrev_i32_e32 v78, 4, v10
	v_and_b32_e32 v10, -16, v10
	v_ashrrev_i32_e32 v15, 31, v14
	s_add_u32 s10, s4, 0xc000400
	v_sub_u32_e32 v21, v187, v10
	v_lshrrev_b32_e32 v15, 28, v15
	s_addc_u32 s11, s5, 0
	v_lshlrev_b32_e32 v162, 3, v21
	v_add_u32_e32 v15, v14, v15
	v_mov_b64_e32 v[12:13], s[10:11]
	v_ashrrev_i32_e32 v163, 31, v162
	v_ashrrev_i32_e32 v79, 4, v15
	v_and_b32_e32 v15, -16, v15
	v_mad_i64_i32 v[8:9], s[10:11], v78, s95, v[12:13]
	v_lshlrev_b64 v[50:51], 1, v[162:163]
	v_sub_u32_e32 v22, v14, v15
	v_lshl_add_u64 v[8:9], v[8:9], 0, v[50:51]
	v_lshlrev_b32_e32 v164, 3, v22
	global_load_dwordx4 v[8:11], v[8:9], off
	v_ashrrev_i32_e32 v165, 31, v164
	v_mad_i64_i32 v[12:13], s[10:11], v79, s95, v[12:13]
	v_lshlrev_b64 v[52:53], 1, v[164:165]
	v_lshl_add_u64 v[12:13], v[12:13], 0, v[52:53]
	global_load_dwordx4 v[12:15], v[12:13], off
	v_ashrrev_i32_e32 v188, 6, v187
	v_lshlrev_b32_e32 v186, 5, v188
	v_and_b32_e32 v185, 31, v49
	s_waitcnt vmcnt(4)
	v_and_b32_e32 v16, 0x60, v186
	v_ashrrev_i32_e32 v23, 8, v187
	v_or3_b32 v18, s37, v16, v185
	v_mov_b64_e32 v[16:17], s[84:85]
	v_mad_i64_i32 v[16:17], s[10:11], v18, s95, v[16:17]
	s_mov_b32 s7, s1
	v_lshlrev_b32_e32 v18, 6, v23
	v_bfe_u32 v184, v49, 5, 1
	v_lshl_add_u64 v[16:17], v[16:17], 0, s[6:7]
	v_ashrrev_i32_e32 v19, 31, v18
	v_lshl_add_u64 v[16:17], v[18:19], 1, v[16:17]
	v_lshlrev_b32_e32 v96, 4, v184
	v_lshl_add_u64 v[16:17], v[16:17], 0, v[96:97]
	global_load_dwordx4 v[110:113], v[16:17], off
	global_load_dwordx4 v[106:109], v[16:17], off offset:32
	global_load_dwordx4 v[102:105], v[16:17], off offset:64
	global_load_dwordx4 v[98:101], v[16:17], off offset:96
	v_and_b32_e32 v18, 0xfffff0, v76
	v_lshlrev_b32_e32 v19, 1, v76
	v_and_or_b32 v18, v19, 8, v18
	v_bfe_u32 v16, v20, 5, 2
	v_lshrrev_b32_e32 v19, 1, v76
	v_lshrrev_b32_e32 v18, 1, v18
	v_and_b32_e32 v20, 3, v76
	v_or_b32_e32 v18, v18, v16
	v_and_or_b32 v19, v19, 4, v20
	v_lshlrev_b32_e32 v56, 4, v49
	v_lshlrev_b32_e32 v18, 9, v18
	v_lshlrev_b32_e32 v19, 6, v19
	v_and_b32_e32 v17, 48, v56
	v_add3_u32 v18, 0, v18, v19
	v_add_u32_e32 v196, v18, v17
	s_waitcnt vmcnt(0)
	v_lshlrev_b32_e32 v32, 3, v23
	v_and_b32_e32 v80, 15, v49
	v_and_b32_e32 v189, 63, v49
	s_mul_i32 s8, s8, 0x1800000
	s_add_u32 s7, s84, s8
	s_addc_u32 s8, s85, 0
	s_add_u32 s41, s7, s6
	v_mad_i64_i32 v[168:169], s[6:7], v76, s95, 0
	v_mad_i64_i32 v[170:171], s[6:7], v77, s95, 0
	v_mad_i64_i32 v[172:173], s[6:7], v78, s95, 0
	v_mad_i64_i32 v[174:175], s[6:7], v79, s95, 0
	s_waitcnt vmcnt(7)
	ds_write_b128 v196, v[0:3]
	v_and_b32_e32 v0, 0xfffff0, v77
	v_lshlrev_b32_e32 v1, 1, v77
	v_and_or_b32 v0, v1, 8, v0
	v_lshrrev_b32_e32 v1, 1, v77
	v_lshrrev_b32_e32 v0, 1, v0
	v_and_b32_e32 v2, 3, v77
	v_or_b32_e32 v0, v0, v16
	v_and_or_b32 v1, v1, 4, v2
	v_lshlrev_b32_e32 v0, 9, v0
	v_lshlrev_b32_e32 v1, 6, v1
	v_add3_u32 v0, 0, v0, v1
	v_bitop3_b32 v1, v78, v21, 15 bitop3:0x6c
	v_add_u32_e32 v197, v0, v17
	v_lshlrev_b32_e32 v0, 8, v78
	v_lshl_add_u32 v1, v1, 4, 0
	v_add_u32_e32 v198, v1, v0
	v_bitop3_b32 v1, v79, v22, 15 bitop3:0x6c
	v_lshlrev_b32_e32 v0, 8, v79
	v_lshl_add_u32 v1, v1, 4, 0
	s_waitcnt vmcnt(6)
	ds_write_b128 v197, v[4:7]
	v_add_u32_e32 v199, v1, v0
	v_bitop3_b32 v0, v32, v80, v184 bitop3:0x36
	s_waitcnt vmcnt(5)
	ds_write_b128 v198, v[8:11] offset:32768
	v_lshlrev_b32_e32 v8, 8, v185
	v_lshl_add_u32 v0, v0, 4, v8
	v_add_u32_e32 v200, 0, v0
	v_not_b32_e32 v4, 63
	v_or_b32_e32 v10, v32, v184
	s_waitcnt vmcnt(4)
	ds_write_b128 v199, v[12:15] offset:32768
	s_waitcnt lgkmcnt(0)
	s_barrier
	ds_read_b128 v[0:3], v200 offset:32768
	v_bitop3_b32 v190, s9, v4, v49 bitop3:0xc8
	ds_read_b128 v[4:7], v200 offset:40960
	s_waitcnt vmcnt(3) lgkmcnt(1)
	v_mfma_f32_32x32x16_bf16 v[16:31], v[0:3], v[110:113], 0
	v_bitop3_b32 v0, v10, v80, 2 bitop3:0x36
	v_lshl_add_u32 v0, v0, 4, v8
	v_add_u32_e32 v201, 0, v0
	ds_read_b128 v[0:3], v201 offset:32768
	v_lshlrev_b32_e32 v9, 3, v189
	s_mov_b64 s[6:7], 0xc0c0800
	s_addc_u32 s42, s8, 0
	s_waitcnt lgkmcnt(1)
	v_mfma_f32_32x32x16_bf16 v[32:47], v[4:7], v[110:113], 0
	v_and_b32_e32 v4, 0xc0, v56
	v_lshlrev_b32_e32 v5, 1, v49
	v_and_or_b32 v4, v9, 24, v4
	v_and_b32_e32 v5, 32, v5
	v_and_b32_e32 v6, 0x100, v9
	v_or3_b32 v49, v4, v5, v6
	ds_read_b128 v[4:7], v201 offset:40960
	s_waitcnt vmcnt(2) lgkmcnt(1)
	v_mfma_f32_32x32x16_bf16 v[16:31], v[0:3], v[106:109], v[16:31]
	v_bitop3_b32 v0, v10, v80, 4 bitop3:0x36
	v_lshl_add_u32 v0, v0, 4, v8
	v_add_u32_e32 v202, 0, v0
	ds_read_b128 v[0:3], v202 offset:32768
	s_add_i32 s89, 0, 0x10000
	s_mov_b32 s8, s1
	s_mov_b32 s9, s1
	s_waitcnt lgkmcnt(1)
	v_mfma_f32_32x32x16_bf16 v[32:47], v[4:7], v[106:109], v[32:47]
	v_lshl_add_u64 v[4:5], v[54:55], 0, s[6:7]
	v_mad_i64_i32 v[6:7], s[6:7], v76, s95, v[4:5]
	v_mad_i64_i32 v[4:5], s[6:7], v77, s95, v[4:5]
	s_add_u32 s6, s4, 0xc0c0400
	s_addc_u32 s7, s5, 0
	global_load_dwordx4 v[56:59], v[6:7], off
	global_load_dwordx4 v[60:63], v[4:5], off
	v_mov_b64_e32 v[4:5], s[6:7]
	s_waitcnt vmcnt(3) lgkmcnt(0)
	v_mfma_f32_32x32x16_bf16 v[16:31], v[0:3], v[102:105], v[16:31]
	v_bitop3_b32 v0, v10, v80, 6 bitop3:0x36
	v_mad_i64_i32 v[6:7], s[6:7], v78, s95, v[4:5]
	v_mad_i64_i32 v[4:5], s[6:7], v79, s95, v[4:5]
	v_lshl_add_u32 v0, v0, 4, v8
	v_lshl_add_u64 v[6:7], v[6:7], 0, v[50:51]
	v_lshl_add_u64 v[4:5], v[4:5], 0, v[52:53]
	v_add_u32_e32 v203, 0, v0
	global_load_dwordx4 v[64:67], v[6:7], off
	global_load_dwordx4 v[68:71], v[4:5], off
	ds_read_b128 v[4:7], v202 offset:40960
	ds_read_b128 v[0:3], v203 offset:32768
	ds_read_b128 v[72:75], v203 offset:40960
	s_waitcnt lgkmcnt(2)
	v_mfma_f32_32x32x16_bf16 v[32:47], v[4:7], v[102:105], v[32:47]
	s_mov_b32 s10, s1
	s_mov_b32 s11, s1
	s_mov_b32 s12, s1
	s_mov_b32 s13, s1
	s_mov_b32 s14, s1
	s_mov_b32 s15, s1
	s_mov_b32 s16, s1
	s_waitcnt vmcnt(4) lgkmcnt(1)
	v_mfma_f32_32x32x16_bf16 v[16:31], v[0:3], v[98:101], v[16:31]
	s_mov_b32 s17, s1
	s_mov_b32 s18, s1
	s_mov_b32 s19, s1
	s_mov_b32 s20, s1
	s_mov_b32 s21, s1
	s_mov_b32 s22, s1
	s_mov_b32 s23, s1
	s_waitcnt lgkmcnt(0)
	v_mfma_f32_32x32x16_bf16 v[32:47], v[72:75], v[98:101], v[32:47]
	s_nop 2
	v_max_f32_e32 v72, v17, v17
	v_max_f32_e32 v73, v16, v16
	v_max_f32_e32 v72, v73, v72
	v_max3_f32 v72, v72, v18, v19
	v_max3_f32 v72, v72, v20, v21
	v_max3_f32 v72, v72, v22, v23
	v_max3_f32 v72, v72, v24, v25
	v_max3_f32 v72, v72, v26, v27
	v_max3_f32 v72, v72, v28, v29
	v_max3_f32 v72, v72, v30, v31
	v_max3_f32 v72, v72, v32, v33
	v_max3_f32 v72, v72, v34, v35
	v_max3_f32 v72, v72, v36, v37
	v_max3_f32 v72, v72, v38, v39
	v_max3_f32 v72, v72, v40, v41
	v_max3_f32 v72, v72, v42, v43
	v_max3_f32 v72, v72, v44, v45
	v_max3_f32 v72, v72, v46, v47
	v_mov_b32_e32 v73, v72
	s_nop 1
	v_permlane32_swap_b32_e32 v72, v73
	v_max_f32_e32 v73, v73, v73
	v_max_f32_e32 v72, v72, v72
	v_mov_b64_e32 v[0:1], s[8:9]
	v_max_f32_e32 v74, v72, v73
	s_cmp_lg_u32 0, -1
	s_mov_b64 s[6:7], 0xc180800
	v_mov_b64_e32 v[2:3], s[10:11]
	v_mov_b64_e32 v[4:5], s[12:13]
	v_mov_b64_e32 v[6:7], s[14:15]
	v_mov_b64_e32 v[8:9], s[16:17]
	v_mov_b64_e32 v[10:11], s[18:19]
	v_mov_b64_e32 v[12:13], s[20:21]
	v_mov_b64_e32 v[14:15], s[22:23]
	v_add_f32_e32 v72, 0x7149f2ca, v74
	s_cselect_b32 s8, 0, 0
	v_lshl_add_u64 v[54:55], v[54:55], 0, s[6:7]
	s_add_u32 s4, s4, 0xc180400
	v_cmp_ge_f32_e32 vcc, s88, v72
	v_mad_i64_i32 v[72:73], s[6:7], v76, s95, v[54:55]
	v_mad_i64_i32 v[54:55], s[6:7], v77, s95, v[54:55]
	s_addc_u32 s5, s5, 0
	global_load_dwordx4 v[114:117], v[72:73], off
	global_load_dwordx4 v[118:121], v[54:55], off
	v_mov_b64_e32 v[54:55], s[4:5]
	v_mad_i64_i32 v[72:73], s[4:5], v78, s95, v[54:55]
	v_lshl_add_u64 v[72:73], v[72:73], 0, v[50:51]
	v_mad_i64_i32 v[54:55], s[4:5], v79, s95, v[54:55]
	v_lshl_add_u64 v[54:55], v[54:55], 0, v[52:53]
	global_load_dwordx4 v[122:125], v[72:73], off
	global_load_dwordx4 v[126:129], v[54:55], off
	s_cmp_eq_u64 vcc, exec
	v_max_f32_e32 v54, 0xf149f2ca, v74
	s_cselect_b64 vcc, -1, 0
	v_cndmask_b32_e32 v205, v54, v219, vcc
	v_sub_f32_e32 v55, 0xf149f2ca, v54
	v_mul_f32_e32 v54, 0xbe38aa3b, v205
	v_fmamk_f32 v16, v16, 0x3e38aa3b, v54
	v_exp_f32_e32 v147, v16
	v_fmamk_f32 v16, v17, 0x3e38aa3b, v54
	v_exp_f32_e32 v159, v16
	v_fmamk_f32 v16, v18, 0x3e38aa3b, v54
	v_exp_f32_e32 v148, v16
	v_fmamk_f32 v16, v19, 0x3e38aa3b, v54
	v_exp_f32_e32 v160, v16
	v_fmamk_f32 v16, v20, 0x3e38aa3b, v54
	v_exp_f32_e32 v149, v16
	v_fmamk_f32 v16, v21, 0x3e38aa3b, v54
	v_exp_f32_e32 v161, v16
	v_fmamk_f32 v16, v22, 0x3e38aa3b, v54
	v_exp_f32_e32 v158, v16
	v_fmamk_f32 v16, v23, 0x3e38aa3b, v54
	v_exp_f32_e32 v230, v16
	v_fmamk_f32 v16, v24, 0x3e38aa3b, v54
	v_exp_f32_e32 v150, v16
	v_fmamk_f32 v16, v25, 0x3e38aa3b, v54
	v_exp_f32_e32 v154, v16
	v_fmamk_f32 v16, v26, 0x3e38aa3b, v54
	v_exp_f32_e32 v151, v16
	v_fmamk_f32 v16, v27, 0x3e38aa3b, v54
	v_exp_f32_e32 v155, v16
	v_fmamk_f32 v16, v28, 0x3e38aa3b, v54
	v_exp_f32_e32 v152, v16
	v_fmamk_f32 v16, v29, 0x3e38aa3b, v54
	v_exp_f32_e32 v156, v16
	v_fmamk_f32 v16, v30, 0x3e38aa3b, v54
	v_mov_b32_e32 v19, 0x1800000
	v_mul_f32_e32 v55, 0x3e38aa3b, v55
	v_exp_f32_e32 v153, v16
	v_mad_u64_u32 v[16:17], s[4:5], s2, v19, v[174:175]
	v_exp_f32_e32 v55, v55
	v_lshl_add_u64 v[16:17], v[16:17], 0, v[52:53]
	v_lshl_add_u64 v[176:177], s[28:29], 0, v[16:17]
	v_mad_u64_u32 v[16:17], s[4:5], s2, v19, v[172:173]
	v_lshl_add_u64 v[16:17], v[16:17], 0, v[50:51]
	v_lshl_add_u64 v[178:179], s[28:29], 0, v[16:17]
	v_mad_u64_u32 v[16:17], s[4:5], s2, v19, v[170:171]
	v_lshlrev_b32_e32 v18, 4, v80
	v_pk_fma_f32 v[130:131], v[46:47], s[90:91], v[54:55] op_sel_hi:[1,0,0]
	v_pk_fma_f32 v[136:137], v[44:45], s[90:91], v[54:55] op_sel_hi:[1,0,0]
	v_pk_fma_f32 v[140:141], v[42:43], s[90:91], v[54:55] op_sel_hi:[1,0,0]
	v_pk_fma_f32 v[132:133], v[40:41], s[90:91], v[54:55] op_sel_hi:[1,0,0]
	v_pk_fma_f32 v[134:135], v[38:39], s[90:91], v[54:55] op_sel_hi:[1,0,0]
	v_pk_fma_f32 v[138:139], v[36:37], s[90:91], v[54:55] op_sel_hi:[1,0,0]
	v_pk_fma_f32 v[142:143], v[34:35], s[90:91], v[54:55] op_sel_hi:[1,0,0]
	v_pk_fma_f32 v[144:145], v[32:33], s[90:91], v[54:55] op_sel_hi:[1,0,0]
	v_fmac_f32_e32 v54, 0x3e38aa3b, v31
	v_or_b32_e32 v16, v16, v18
	v_exp_f32_e32 v157, v54
	v_lshl_add_u64 v[180:181], s[30:31], 0, v[16:17]
	v_mad_u64_u32 v[16:17], s[4:5], s2, v19, v[168:169]
	v_lshl_add_u32 v81, v190, 2, s89
	v_add_u32_e32 v195, s8, v49
	s_waitcnt vmcnt(4)
	s_addk_i32 s8, 0x4000
	v_or_b32_e32 v16, v16, v18
	s_waitcnt vmcnt(7)
	ds_write_b128 v196, v[56:59] offset:16384
	s_waitcnt vmcnt(6)
	ds_write_b128 v197, v[60:63] offset:16384
	s_waitcnt vmcnt(5)
	ds_write_b128 v198, v[64:67] offset:49152
	s_waitcnt vmcnt(4)
	ds_write_b128 v199, v[68:71] offset:49152
	v_cndmask_b32_e64 v204, v55, 1.0, vcc
	v_add_u32_e32 v194, s8, v49
	v_add_u32_e32 v191, v81, v96
	v_lshl_add_u64 v[182:183], s[30:31], 0, v[16:17]
	v_lshlrev_b32_e32 v96, 1, v48
	v_mov_b64_e32 v[30:31], v[14:15]
	v_mov_b64_e32 v[46:47], v[14:15]
	v_mov_b64_e32 v[62:63], v[14:15]
	s_mov_b32 s12, -1
	v_cmp_gt_u32_e64 s[6:7], 32, v189
	v_lshl_add_u32 v192, v185, 2, v81
	v_mov_b32_e32 v193, 0
	v_mov_b64_e32 v[28:29], v[12:13]
	v_mov_b64_e32 v[26:27], v[10:11]
	v_mov_b64_e32 v[24:25], v[8:9]
	v_mov_b64_e32 v[22:23], v[6:7]
	v_mov_b64_e32 v[20:21], v[4:5]
	v_mov_b64_e32 v[18:19], v[2:3]
	v_mov_b64_e32 v[16:17], v[0:1]
	v_mov_b64_e32 v[44:45], v[12:13]
	v_mov_b64_e32 v[42:43], v[10:11]
	v_mov_b64_e32 v[40:41], v[8:9]
	v_mov_b64_e32 v[38:39], v[6:7]
	v_mov_b64_e32 v[36:37], v[4:5]
	v_mov_b64_e32 v[34:35], v[2:3]
	v_mov_b64_e32 v[32:33], v[0:1]
	v_mov_b64_e32 v[60:61], v[12:13]
	v_mov_b64_e32 v[58:59], v[10:11]
	v_mov_b64_e32 v[56:57], v[8:9]
	v_mov_b64_e32 v[54:55], v[6:7]
	v_mov_b64_e32 v[52:53], v[4:5]
	v_mov_b64_e32 v[50:51], v[2:3]
	v_mov_b64_e32 v[48:49], v[0:1]
	s_waitcnt lgkmcnt(0)
	s_barrier
	.p2align 6

.LBB0_709:
	s_or_b64 exec, exec, s[4:5]
	s_and_b32 s2, s0, 7
	s_lshl_b32 s2, s2, 8
	v_and_b32_e32 v1, 63, v5
	s_add_i32 s86, s2, 0x3e40
	v_and_b32_e32 v2, 0x3fffffc0, v7
	s_add_i32 s4, 0, 0x8000
	v_lshl_add_u32 v152, v2, 2, s3
	v_lshlrev_b32_e32 v2, 6, v7
	s_cmp_lg_u32 s4, -1
	v_lshlrev_b32_e32 v10, 4, v1
	v_and_b32_e32 v2, 0xffffc000, v2
	s_cselect_b32 s4, s4, 0
	v_lshlrev_b32_e32 v9, 3, v1
	v_and_b32_e32 v10, 0xc0, v10
	v_lshlrev_b32_e32 v11, 1, v1
	v_add_u32_e32 v2, s4, v2
	v_lshlrev_b32_e32 v3, 10, v6
	v_and_or_b32 v10, v9, 24, v10
	v_and_b32_e32 v11, 32, v11
	v_and_b32_e32 v9, 0x100, v9
	s_lshl_b32 s4, s83, 6
	v_and_b32_e32 v8, 0x400, v3
	v_or3_b32 v9, v10, v11, v9
	s_or_b32 s8, s4, s82
	s_and_b32 s4, s94, 0xffffff00
	v_ashrrev_i32_e32 v164, 5, v7
	v_add3_u32 v162, v2, v8, v9
	s_ashr_i32 s5, s4, 31
	v_lshlrev_b32_e32 v2, 3, v5
	v_add_u32_e32 v10, s8, v164
	v_mov_b64_e32 v[8:9], s[84:85]
	v_and_b32_e32 v2, 0xf8, v2
	v_mad_i64_i32 v[10:11], s[6:7], v10, s95, v[8:9]
	s_lshl_b64 s[4:5], s[4:5], 1
	v_lshlrev_b32_e32 v96, 1, v2
	v_lshl_add_u64 v[10:11], v[10:11], 0, s[4:5]
	v_lshl_add_u64 v[10:11], v[10:11], 0, v[96:97]
	s_movk_i32 s9, 0x2000
	v_add_co_u32_e32 v10, vcc, s9, v10
	v_and_b32_e32 v16, 0xfffff0, v164
	s_nop 0
	v_addc_co_u32_e32 v11, vcc, 0, v11, vcc
	global_load_dwordx4 v[80:83], v[10:11], off
	global_load_dwordx4 v[84:87], v[10:11], off offset:1024
	v_add_u32_e32 v10, 0x200, v7
	v_ashrrev_i32_e32 v168, 5, v10
	v_add_u32_e32 v10, s8, v168
	v_mad_i64_i32 v[10:11], s[6:7], v10, s95, v[8:9]
	v_lshl_add_u64 v[10:11], v[10:11], 0, s[4:5]
	v_lshl_add_u64 v[10:11], v[10:11], 0, v[96:97]
	v_add_co_u32_e32 v10, vcc, s9, v10
	v_lshlrev_b32_e32 v17, 1, v164
	s_nop 0
	v_addc_co_u32_e32 v11, vcc, 0, v11, vcc
	global_load_dwordx4 v[88:91], v[10:11], off
	global_load_dwordx4 v[92:95], v[10:11], off offset:1024
	v_add_u32_e32 v10, 0x400, v7
	v_ashrrev_i32_e32 v170, 5, v10
	v_add_u32_e32 v10, s8, v170
	v_add_u32_e32 v7, 0x600, v7
	v_mad_i64_i32 v[10:11], s[6:7], v10, s95, v[8:9]
	v_ashrrev_i32_e32 v173, 5, v7
	v_lshl_add_u64 v[10:11], v[10:11], 0, s[4:5]
	v_add_u32_e32 v7, s8, v173
	v_lshl_add_u64 v[10:11], v[10:11], 0, v[96:97]
	v_mad_i64_i32 v[8:9], s[6:7], v7, s95, v[8:9]
	v_add_co_u32_e32 v10, vcc, s9, v10
	v_lshl_add_u64 v[8:9], v[8:9], 0, s[4:5]
	s_nop 0
	v_addc_co_u32_e32 v11, vcc, 0, v11, vcc
	v_lshl_add_u64 v[8:9], v[8:9], 0, v[96:97]
	v_add_co_u32_e32 v8, vcc, s9, v8
	v_and_b32_e32 v19, 0xfffff0, v168
	v_lshlrev_b32_e32 v20, 1, v168
	v_and_b32_e32 v22, 0xfffff0, v170
	v_lshlrev_b32_e32 v23, 1, v170
	v_and_b32_e32 v25, 0xfffff0, v173
	v_lshlrev_b32_e32 v26, 1, v173
	v_addc_co_u32_e32 v9, vcc, 0, v9, vcc
	v_and_or_b32 v16, v17, 8, v16
	v_and_or_b32 v19, v20, 8, v19
	v_and_or_b32 v22, v23, 8, v22
	v_and_or_b32 v25, v26, 8, v25
	global_load_dwordx4 v[98:101], v[10:11], off
	global_load_dwordx4 v[102:105], v[10:11], off offset:1024
	global_load_dwordx4 v[106:109], v[8:9], off
	global_load_dwordx4 v[110:113], v[8:9], off offset:1024
	v_bfe_u32 v8, v5, 2, 2
	v_lshrrev_b32_e32 v16, 1, v16
	v_lshrrev_b32_e32 v19, 1, v19
	v_lshrrev_b32_e32 v22, 1, v22
	v_lshrrev_b32_e32 v25, 1, v25
	v_lshlrev_b32_e32 v7, 10, v155
	v_cmp_gt_u32_e64 s[6:7], 32, v1
	v_or_b32_e32 v1, v4, v155
	v_lshrrev_b32_e32 v17, 1, v164
	v_or_b32_e32 v16, v16, v8
	v_and_b32_e32 v18, 3, v164
	v_lshrrev_b32_e32 v20, 1, v168
	v_or_b32_e32 v19, v19, v8
	v_and_b32_e32 v21, 3, v168
	v_lshrrev_b32_e32 v23, 1, v170
	v_or_b32_e32 v22, v22, v8
	v_and_b32_e32 v24, 3, v170
	v_lshrrev_b32_e32 v26, 1, v173
	v_or_b32_e32 v8, v25, v8
	v_and_b32_e32 v25, 3, v173
	v_and_b32_e32 v7, 0x4000, v7
	v_max_i32_e32 v1, 8, v1
	v_and_or_b32 v17, v17, 4, v18
	v_and_or_b32 v20, v20, 4, v21
	v_and_or_b32 v23, v23, 4, v24
	v_and_or_b32 v25, v26, 4, v25
	v_add_u32_e32 v7, 0, v7
	v_add_u32_e32 v1, -8, v1
	v_lshlrev_b32_e32 v171, 2, v151
	v_lshlrev_b32_e32 v16, 9, v16
	v_lshlrev_b32_e32 v17, 6, v17
	v_lshlrev_b32_e32 v19, 9, v19
	v_lshlrev_b32_e32 v20, 6, v20
	v_lshlrev_b32_e32 v22, 9, v22
	v_lshlrev_b32_e32 v23, 6, v23
	v_lshlrev_b32_e32 v8, 9, v8
	v_lshlrev_b32_e32 v25, 6, v25
	v_min_u32_e32 v1, 48, v1
	v_add3_u32 v16, v7, v16, v17
	v_add3_u32 v19, v7, v19, v20
	v_add3_u32 v22, v7, v22, v23
	v_add3_u32 v7, v7, v8, v25
	v_or_b32_e32 v159, 16, v171
	v_or_b32_e32 v25, 32, v171
	v_cmp_lt_u32_e32 vcc, v159, v1
	v_or_b32_e32 v8, 33, v171
	v_cmp_ge_u32_e64 s[10:11], v25, v1
	v_or_b32_e32 v158, 17, v171
	s_and_b64 s[10:11], s[10:11], vcc
	v_cmp_ge_u32_e32 vcc, v8, v1
	v_cmp_lt_u32_e64 s[12:13], v158, v1
	v_or_b32_e32 v157, 18, v171
	v_or_b32_e32 v27, 34, v171
	s_and_b64 s[12:13], vcc, s[12:13]
	v_cmp_lt_u32_e32 vcc, v157, v1
	v_or_b32_e32 v26, 35, v171
	v_cmp_ge_u32_e64 s[18:19], v27, v1
	v_or_b32_e32 v154, 19, v171
	s_and_b64 s[18:19], s[18:19], vcc
	v_cmp_ge_u32_e32 vcc, v26, v1
	v_cmp_lt_u32_e64 s[20:21], v154, v1
	v_or_b32_e32 v153, 24, v171
	v_or_b32_e32 v29, 40, v171
	s_and_b64 s[20:21], vcc, s[20:21]
	v_cmp_lt_u32_e32 vcc, v153, v1
	v_or_b32_e32 v28, 41, v171
	v_cmp_ge_u32_e64 s[26:27], v29, v1
	v_or_b32_e32 v150, 25, v171
	s_and_b64 s[26:27], s[26:27], vcc
	v_cmp_ge_u32_e32 vcc, v28, v1
	v_cmp_lt_u32_e64 s[28:29], v150, v1
	v_or_b32_e32 v149, 26, v171
	v_or_b32_e32 v31, 42, v171
	v_lshlrev_b32_e32 v6, 3, v6
	s_and_b64 s[28:29], vcc, s[28:29]
	v_cmp_lt_u32_e32 vcc, v149, v1
	v_or_b32_e32 v30, 43, v171
	v_cmp_ge_u32_e64 s[36:37], v31, v1
	v_or_b32_e32 v148, 27, v171
	v_lshlrev_b32_e32 v9, 4, v5
	v_or_b32_e32 v10, v6, v151
	v_and_b32_e32 v5, 15, v5
	s_and_b64 s[36:37], s[36:37], vcc
	v_cmp_ge_u32_e32 vcc, v30, v1
	v_cmp_lt_u32_e64 s[40:41], v148, v1
	v_bitop3_b32 v6, v6, v5, v151 bitop3:0x36
	v_bitop3_b32 v12, v10, v5, 2 bitop3:0x36
	v_bitop3_b32 v13, v10, v5, 4 bitop3:0x36
	v_bitop3_b32 v5, v10, v5, 6 bitop3:0x36
	v_add_u32_e32 v10, 16, v1
	v_cmp_lt_u32_e64 s[8:9], v171, v1
	s_and_b64 s[40:41], vcc, s[40:41]
	v_cmp_ge_u32_e32 vcc, v159, v1
	s_and_b64 s[42:43], vcc, s[8:9]
	v_cmp_ge_u32_e32 vcc, v158, v1
	v_cmp_lt_u32_e64 s[44:45], v158, v10
	s_and_b64 s[44:45], vcc, s[44:45]
	v_cmp_ge_u32_e32 vcc, v157, v1
	v_cmp_lt_u32_e64 s[50:51], v157, v10
	s_and_b64 s[50:51], vcc, s[50:51]
	v_cmp_ge_u32_e32 vcc, v154, v1
	v_cmp_lt_u32_e64 s[52:53], v154, v10
	s_and_b64 s[52:53], vcc, s[52:53]
	v_cmp_ge_u32_e32 vcc, v153, v1
	v_cmp_lt_u32_e64 s[58:59], v153, v10
	s_and_b64 s[58:59], vcc, s[58:59]
	v_cmp_ge_u32_e32 vcc, v150, v1
	v_cmp_lt_u32_e64 s[60:61], v150, v10
	v_or_b32_e32 v172, 2, v171
	v_or_b32_e32 v174, 1, v171
	v_or_b32_e32 v165, 8, v171
	v_or_b32_e32 v169, 3, v171
	v_or_b32_e32 v161, 10, v171
	v_or_b32_e32 v163, 9, v171
	v_or_b32_e32 v160, 11, v171
	s_and_b64 s[60:61], vcc, s[60:61]
	v_cmp_ge_u32_e32 vcc, v149, v1
	v_cmp_lt_u32_e64 s[66:67], v149, v10
	v_cmp_lt_u32_e64 s[14:15], v172, v1
	v_cmp_lt_u32_e64 s[16:17], v174, v1
	v_cmp_lt_u32_e64 s[22:23], v165, v1
	v_cmp_lt_u32_e64 s[24:25], v169, v1
	v_cmp_lt_u32_e64 s[30:31], v161, v1
	v_cmp_lt_u32_e64 s[34:35], v163, v1
	v_cmp_lt_u32_e64 s[38:39], v160, v1
	v_cmp_lt_u32_e64 s[46:47], v8, v1
	v_cmp_lt_u32_e64 s[48:49], v25, v1
	v_cmp_lt_u32_e64 s[54:55], v26, v1
	v_cmp_lt_u32_e64 s[56:57], v27, v1
	v_cmp_lt_u32_e64 s[62:63], v28, v1
	v_cmp_lt_u32_e64 s[64:65], v29, v1
	s_and_b64 s[66:67], vcc, s[66:67]
	v_cmp_ge_u32_e32 vcc, v148, v1
	v_cmp_lt_u32_e64 s[70:71], v30, v1
	v_cmp_lt_u32_e64 s[72:73], v31, v1
	v_sub_u32_e32 v1, v171, v155
	v_sub_u32_e32 v1, v1, v4
	v_cmp_lt_u32_e64 s[68:69], v148, v10
	v_add_u32_e32 v10, 0x4a, v1
	v_min_u32_e32 v10, 31, v10
	v_lshl_or_b32 v10, v10, 2, v3
	v_add_u32_e32 v176, s89, v10
	v_add_u32_e32 v10, 27, v1
	v_max_i32_e32 v10, -15, v10
	v_add_u32_e32 v10, 15, v10
	v_min_u32_e32 v10, 31, v10
	v_lshl_or_b32 v10, v10, 2, v3
	v_add_u32_e32 v177, s89, v10
	v_add_u32_e32 v10, 0x49, v1
	v_min_u32_e32 v10, 31, v10
	v_lshl_or_b32 v10, v10, 2, v3
	v_add_u32_e32 v178, s89, v10
	v_add_u32_e32 v10, 26, v1
	v_max_i32_e32 v10, -15, v10
	v_add_u32_e32 v10, 15, v10
	v_min_u32_e32 v10, 31, v10
	v_lshl_or_b32 v10, v10, 2, v3
	v_add_u32_e32 v179, s89, v10
	v_add_u32_e32 v10, 0x48, v1
	v_min_u32_e32 v10, 31, v10
	v_lshl_or_b32 v10, v10, 2, v3
	v_add_u32_e32 v180, s89, v10
	v_add_u32_e32 v10, 25, v1
	v_max_i32_e32 v10, -15, v10
	v_add_u32_e32 v10, 15, v10
	v_min_u32_e32 v10, 31, v10
	v_lshl_or_b32 v10, v10, 2, v3
	v_add_u32_e32 v181, s89, v10
	v_add_u32_e32 v10, 0x47, v1
	v_min_u32_e32 v10, 31, v10
	v_lshl_or_b32 v10, v10, 2, v3
	v_add_u32_e32 v182, s89, v10
	v_add_u32_e32 v10, 24, v1
	v_max_i32_e32 v10, -15, v10
	v_add_u32_e32 v10, 15, v10
	v_min_u32_e32 v10, 31, v10
	v_lshl_or_b32 v10, v10, 2, v3
	v_add_u32_e32 v183, s89, v10
	v_add_u32_e32 v10, 0x42, v1
	v_min_u32_e32 v10, 31, v10
	v_lshl_or_b32 v10, v10, 2, v3
	v_add_u32_e32 v184, s89, v10
	v_add_u32_e32 v10, 19, v1
	v_max_i32_e32 v10, -15, v10
	v_add_u32_e32 v10, 15, v10
	v_min_u32_e32 v10, 31, v10
	v_lshl_or_b32 v10, v10, 2, v3
	v_add_u32_e32 v185, s89, v10
	v_add_u32_e32 v10, 0x41, v1
	v_min_u32_e32 v10, 31, v10
	v_lshl_or_b32 v10, v10, 2, v3
	v_add_u32_e32 v186, s89, v10
	v_add_u32_e32 v10, 18, v1
	v_max_i32_e32 v10, -15, v10
	v_add_u32_e32 v10, 15, v10
	v_min_u32_e32 v10, 31, v10
	v_lshl_or_b32 v10, v10, 2, v3
	v_add_u32_e32 v187, s89, v10
	v_add_u32_e32 v10, 64, v1
	v_min_u32_e32 v10, 31, v10
	v_lshl_or_b32 v10, v10, 2, v3
	v_add_u32_e32 v188, s89, v10
	v_add_u32_e32 v10, 17, v1
	v_max_i32_e32 v10, -15, v10
	v_add_u32_e32 v10, 15, v10
	v_min_u32_e32 v10, 31, v10
	v_lshl_or_b32 v10, v10, 2, v3
	v_add_u32_e32 v189, s89, v10
	v_add_u32_e32 v10, 63, v1
	v_min_u32_e32 v10, 31, v10
	v_lshl_or_b32 v10, v10, 2, v3
	v_add_u32_e32 v190, s89, v10
	v_add_u32_e32 v10, 16, v1
	v_max_i32_e32 v10, -15, v10
	v_add_u32_e32 v10, 15, v10
	v_min_u32_e32 v10, 31, v10
	v_lshl_or_b32 v10, v10, 2, v3
	v_add_u32_e32 v191, s89, v10
	v_sub_u32_e32 v10, v30, v155
	v_sub_u32_e32 v10, v10, v4
	v_max_i32_e32 v10, -15, v10
	v_add_u32_e32 v10, 15, v10
	v_min_u32_e32 v10, 31, v10
	v_lshl_or_b32 v10, v10, 2, v3
	v_add_u32_e32 v192, s89, v10
	v_add_u32_e32 v10, 11, v1
	v_max_i32_e32 v10, -15, v10
	v_add_u32_e32 v10, 15, v10
	v_min_u32_e32 v10, 31, v10
	v_lshl_or_b32 v10, v10, 2, v3
	v_add_u32_e32 v193, s89, v10
	v_sub_u32_e32 v10, v31, v155
	v_sub_u32_e32 v10, v10, v4
	v_max_i32_e32 v10, -15, v10
	v_add_u32_e32 v10, 15, v10
	v_min_u32_e32 v10, 31, v10
	v_lshl_or_b32 v10, v10, 2, v3
	v_add_u32_e32 v194, s89, v10
	v_sub_u32_e32 v10, v161, v155
	v_sub_u32_e32 v10, v10, v4
	v_max_i32_e32 v10, -15, v10
	v_add_u32_e32 v10, 15, v10
	v_min_u32_e32 v10, 31, v10
	v_lshl_or_b32 v10, v10, 2, v3
	v_add_u32_e32 v195, s89, v10
	v_sub_u32_e32 v10, v28, v155
	v_sub_u32_e32 v10, v10, v4
	v_max_i32_e32 v10, -15, v10
	v_add_u32_e32 v10, 15, v10
	v_min_u32_e32 v10, 31, v10
	v_lshl_or_b32 v10, v10, 2, v3
	v_add_u32_e32 v196, s89, v10
	v_sub_u32_e32 v10, v163, v155
	v_sub_u32_e32 v10, v10, v4
	v_max_i32_e32 v10, -15, v10
	v_add_u32_e32 v10, 15, v10
	v_min_u32_e32 v10, 31, v10
	v_lshl_or_b32 v10, v10, 2, v3
	v_add_u32_e32 v197, s89, v10
	v_sub_u32_e32 v10, v29, v155
	v_sub_u32_e32 v10, v10, v4
	v_max_i32_e32 v10, -15, v10
	v_add_u32_e32 v10, 15, v10
	v_min_u32_e32 v10, 31, v10
	v_lshl_or_b32 v10, v10, 2, v3
	v_add_u32_e32 v198, s89, v10
	v_sub_u32_e32 v10, v165, v155
	v_sub_u32_e32 v10, v10, v4
	v_max_i32_e32 v10, -15, v10
	v_add_u32_e32 v10, 15, v10
	v_min_u32_e32 v10, 31, v10
	v_lshl_or_b32 v10, v10, 2, v3
	v_add_u32_e32 v199, s89, v10
	v_sub_u32_e32 v10, v26, v155
	v_sub_u32_e32 v10, v10, v4
	v_max_i32_e32 v10, -15, v10
	v_add_u32_e32 v10, 15, v10
	v_min_u32_e32 v10, 31, v10
	v_lshl_or_b32 v10, v10, 2, v3
	v_add_u32_e32 v200, s89, v10
	v_sub_u32_e32 v10, v169, v155
	v_sub_u32_e32 v8, v8, v155
	v_sub_u32_e32 v10, v10, v4
	v_sub_u32_e32 v8, v8, v4
	v_max_i32_e32 v10, -15, v10
	v_max_i32_e32 v8, -15, v8
	v_add_u32_e32 v10, 15, v10
	v_add_u32_e32 v8, 15, v8
	v_min_u32_e32 v10, 31, v10
	v_min_u32_e32 v8, 31, v8
	v_lshl_or_b32 v10, v10, 2, v3
	v_lshl_or_b32 v8, v8, 2, v3
	v_add_u32_e32 v201, s89, v10
	v_sub_u32_e32 v10, v27, v155
	v_add_u32_e32 v204, s89, v8
	v_sub_u32_e32 v8, v174, v155
	v_sub_u32_e32 v10, v10, v4
	v_sub_u32_e32 v8, v8, v4
	v_max_i32_e32 v10, -15, v10
	v_max_i32_e32 v8, -15, v8
	v_add_u32_e32 v10, 15, v10
	v_add_u32_e32 v8, 15, v8
	v_min_u32_e32 v10, 31, v10
	v_min_u32_e32 v8, 31, v8
	v_lshl_or_b32 v10, v10, 2, v3
	v_lshl_or_b32 v8, v8, 2, v3
	v_add_u32_e32 v202, s89, v10
	v_sub_u32_e32 v10, v172, v155
	v_add_u32_e32 v205, s89, v8
	v_sub_u32_e32 v8, v25, v155
	v_sub_u32_e32 v10, v10, v4
	v_sub_u32_e32 v4, v8, v4
	v_max_i32_e32 v10, -15, v10
	v_max_i32_e32 v4, -15, v4
	v_max_i32_e32 v1, -15, v1
	v_add_u32_e32 v10, 15, v10
	v_add_u32_e32 v4, 15, v4
	v_add_u32_e32 v1, 15, v1
	v_bitop3_b32 v15, v164, v155, 15 bitop3:0x6c
	v_bitop3_b32 v18, v168, v155, 15 bitop3:0x6c
	v_bitop3_b32 v21, v170, v155, 15 bitop3:0x6c
	v_bitop3_b32 v24, v173, v155, 15 bitop3:0x6c
	v_min_u32_e32 v10, 31, v10
	v_min_u32_e32 v4, 31, v4
	v_min_u32_e32 v1, 31, v1
	v_and_b32_e32 v9, 48, v9
	v_lshl_add_u32 v11, v155, 9, 0
	v_lshlrev_b32_e32 v6, 4, v6
	v_lshlrev_b32_e32 v12, 4, v12
	v_lshlrev_b32_e32 v13, 4, v13
	v_lshlrev_b32_e32 v5, 4, v5
	v_lshlrev_b32_e32 v14, 9, v164
	v_lshl_add_u32 v15, v15, 4, 0
	v_lshlrev_b32_e32 v17, 9, v168
	v_lshl_add_u32 v18, v18, 4, 0
	v_lshlrev_b32_e32 v20, 9, v170
	v_lshl_add_u32 v21, v21, 4, 0
	v_lshlrev_b32_e32 v23, 9, v173
	v_lshl_add_u32 v24, v24, 4, 0
	v_lshl_or_b32 v10, v10, 2, v3
	v_lshl_or_b32 v4, v4, 2, v3
	v_lshl_or_b32 v1, v1, 2, v3
	v_mov_b32_e32 v240, 0
	s_mov_b32 s2, 0
	v_lshl_add_u32 v175, v155, 2, v152
	s_and_b64 s[68:69], vcc, s[68:69]
	v_add_u32_e32 v203, s89, v10
	v_add_u32_e32 v206, s89, v4
	v_add_u32_e32 v207, s89, v1
	v_mov_b32_e32 v241, 0xf149f2ca
	s_movk_i32 s87, 0xfa00
	v_add_u32_e32 v227, v15, v14
	v_add_u32_e32 v228, v16, v9
	v_add_u32_e32 v229, v18, v17
	v_add_u32_e32 v230, v19, v9
	v_add_u32_e32 v231, v21, v20
	v_add_u32_e32 v232, v22, v9
	v_add_u32_e32 v233, v24, v23
	v_add_u32_e32 v234, v7, v9
	v_lshlrev_b32_e32 v96, 1, v2
	v_add_u32_e32 v235, v11, v6
	v_add_u32_e32 v236, v11, v12
	v_add_u32_e32 v237, v11, v13
	v_add_u32_e32 v238, v11, v5
	v_add_u32_e32 v239, v152, v0
	v_mov_b32_e32 v0, 0
	v_mov_b32_e32 v1, v240
	v_mov_b32_e32 v2, v240
	v_mov_b32_e32 v3, v240
	v_mov_b32_e32 v4, v240
	v_mov_b32_e32 v5, v240
	v_mov_b32_e32 v6, v240
	v_mov_b32_e32 v7, v240
	v_mov_b32_e32 v8, v240
	v_mov_b32_e32 v9, v240
	v_mov_b32_e32 v10, v240
	v_mov_b32_e32 v11, v240
	v_mov_b32_e32 v12, v240
	v_mov_b32_e32 v13, v240
	v_mov_b32_e32 v14, v240
	v_mov_b32_e32 v15, v240
	v_mov_b32_e32 v16, 0
	v_mov_b32_e32 v17, v240
	v_mov_b32_e32 v18, v240
	v_mov_b32_e32 v19, v240
	v_mov_b32_e32 v20, v240
	v_mov_b32_e32 v21, v240
	v_mov_b32_e32 v22, v240
	v_mov_b32_e32 v23, v240
	v_mov_b32_e32 v24, v240
	v_mov_b32_e32 v25, v240
	v_mov_b32_e32 v26, v240
	v_mov_b32_e32 v27, v240
	v_mov_b32_e32 v28, v240
	v_mov_b32_e32 v29, v240
	v_mov_b32_e32 v30, v240
	v_mov_b32_e32 v31, v240
	.p2align 6

.LBB0_1357:
	v_mov_b64_e32 v[0:1], s[12:13]
	v_cmp_lt_i64_e32 vcc, s[10:11], v[0:1]
	s_lshl_b32 s19, s18, 20
	s_lshl_b32 s10, s16, 10
	s_add_i32 s19, s19, s10
	s_and_b64 s[10:11], vcc, exec
	s_cselect_b32 s15, s19, s45
	s_lshl_b32 s43, s17, 18
	s_lshl_b32 s10, s16, 21
	s_add_i32 s43, s43, s10
	s_and_b64 s[10:11], vcc, exec
	v_mov_b32_e32 v0, 0
	s_cselect_b32 s44, s43, s46
	s_add_i32 s45, s45, 0x80080
	s_addk_i32 s46, 0x100
	s_mov_b32 s47, -2
	v_mov_b32_e32 v1, v0
	v_mov_b32_e32 v2, v0
	v_mov_b32_e32 v3, v0
	v_mov_b32_e32 v4, v0
	v_mov_b32_e32 v5, v0
	v_mov_b32_e32 v6, v0
	v_mov_b32_e32 v7, v0
	v_mov_b32_e32 v8, v0
	v_mov_b32_e32 v9, v0
	v_mov_b32_e32 v10, v0
	v_mov_b32_e32 v11, v0
	v_mov_b32_e32 v12, v0
	v_mov_b32_e32 v13, v0
	v_mov_b32_e32 v14, v0
	v_mov_b32_e32 v15, v0
	v_mov_b32_e32 v24, v0
	v_mov_b32_e32 v25, v0
	v_mov_b32_e32 v26, v0
	v_mov_b32_e32 v27, v0
	v_mov_b32_e32 v28, v0
	v_mov_b32_e32 v29, v0
	v_mov_b32_e32 v30, v0
	v_mov_b32_e32 v31, v0
	v_mov_b32_e32 v40, v0
	v_mov_b32_e32 v41, v0
	v_mov_b32_e32 v42, v0
	v_mov_b32_e32 v43, v0
	v_mov_b32_e32 v44, v0
	v_mov_b32_e32 v45, v0
	v_mov_b32_e32 v46, v0
	v_mov_b32_e32 v47, v0
	v_mov_b32_e32 v16, v0
	v_mov_b32_e32 v17, v0
	v_mov_b32_e32 v18, v0
	v_mov_b32_e32 v19, v0
	v_mov_b32_e32 v20, v0
	v_mov_b32_e32 v21, v0
	v_mov_b32_e32 v22, v0
	v_mov_b32_e32 v23, v0
	v_mov_b32_e32 v32, v0
	v_mov_b32_e32 v33, v0
	v_mov_b32_e32 v34, v0
	v_mov_b32_e32 v35, v0
	v_mov_b32_e32 v36, v0
	v_mov_b32_e32 v37, v0
	v_mov_b32_e32 v38, v0
	v_mov_b32_e32 v39, v0
	v_mov_b32_e32 v48, v0
	v_mov_b32_e32 v49, v0
	v_mov_b32_e32 v50, v0
	v_mov_b32_e32 v51, v0
	v_mov_b32_e32 v52, v0
	v_mov_b32_e32 v53, v0
	v_mov_b32_e32 v54, v0
	v_mov_b32_e32 v55, v0
	v_mov_b32_e32 v56, v0
	v_mov_b32_e32 v57, v0
	v_mov_b32_e32 v58, v0
	v_mov_b32_e32 v59, v0
	v_mov_b32_e32 v60, v0
	v_mov_b32_e32 v61, v0
	v_mov_b32_e32 v62, v0
	v_mov_b32_e32 v63, v0
	v_mov_b32_e32 v64, v0
	v_mov_b32_e32 v65, v0
	v_mov_b32_e32 v66, v0
	v_mov_b32_e32 v67, v0
	v_mov_b32_e32 v68, v0
	v_mov_b32_e32 v69, v0
	v_mov_b32_e32 v70, v0
	v_mov_b32_e32 v71, v0
	v_mov_b32_e32 v72, v0
	v_mov_b32_e32 v73, v0
	v_mov_b32_e32 v74, v0
	v_mov_b32_e32 v75, v0
	v_mov_b32_e32 v76, v0
	v_mov_b32_e32 v77, v0
	v_mov_b32_e32 v78, v0
	v_mov_b32_e32 v79, v0
	v_mov_b32_e32 v88, v0
	v_mov_b32_e32 v89, v0
	v_mov_b32_e32 v90, v0
	v_mov_b32_e32 v91, v0
	v_mov_b32_e32 v92, v0
	v_mov_b32_e32 v93, v0
	v_mov_b32_e32 v94, v0
	v_mov_b32_e32 v95, v0
	v_mov_b32_e32 v106, v0
	v_mov_b32_e32 v107, v0
	v_mov_b32_e32 v108, v0
	v_mov_b32_e32 v109, v0
	v_mov_b32_e32 v110, v0
	v_mov_b32_e32 v111, v0
	v_mov_b32_e32 v112, v0
	v_mov_b32_e32 v113, v0
	v_mov_b32_e32 v80, v0
	v_mov_b32_e32 v81, v0
	v_mov_b32_e32 v82, v0
	v_mov_b32_e32 v83, v0
	v_mov_b32_e32 v84, v0
	v_mov_b32_e32 v85, v0
	v_mov_b32_e32 v86, v0
	v_mov_b32_e32 v87, v0
	v_mov_b32_e32 v98, v0
	v_mov_b32_e32 v99, v0
	v_mov_b32_e32 v100, v0
	v_mov_b32_e32 v101, v0
	v_mov_b32_e32 v102, v0
	v_mov_b32_e32 v103, v0
	v_mov_b32_e32 v104, v0
	v_mov_b32_e32 v105, v0
	v_mov_b32_e32 v114, v0
	v_mov_b32_e32 v115, v0
	v_mov_b32_e32 v116, v0
	v_mov_b32_e32 v117, v0
	v_mov_b32_e32 v118, v0
	v_mov_b32_e32 v119, v0
	v_mov_b32_e32 v120, v0
	v_mov_b32_e32 v121, v0
	v_mov_b32_e32 v122, v0
	v_mov_b32_e32 v123, v0
	v_mov_b32_e32 v124, v0
	v_mov_b32_e32 v125, v0
	v_mov_b32_e32 v126, v0
	v_mov_b32_e32 v127, v0
	v_mov_b32_e32 v128, v0
	v_mov_b32_e32 v129, v0
	.p2align 6

.LBB0_1426:
	v_mov_b64_e32 v[0:1], s[6:7]
	v_cmp_lt_i64_e32 vcc, s[10:11], v[0:1]
	s_lshl_b32 s22, s21, 19
	s_and_b64 s[10:11], vcc, exec
	s_cselect_b32 s19, s22, s46
	s_lshl_b32 s23, s20, 19
	s_and_b64 s[10:11], vcc, exec
	v_mov_b32_e32 v0, 0
	s_cselect_b32 s45, s23, s47
	s_add_i32 s46, s46, 0x40080
	s_addk_i32 s47, 0x100
	s_mov_b32 s48, -2
	v_mov_b32_e32 v1, v0
	v_mov_b32_e32 v2, v0
	v_mov_b32_e32 v3, v0
	v_mov_b32_e32 v4, v0
	v_mov_b32_e32 v5, v0
	v_mov_b32_e32 v6, v0
	v_mov_b32_e32 v7, v0
	s_waitcnt vmcnt(14)
	v_mov_b32_e32 v16, v0
	v_mov_b32_e32 v17, v0
	v_mov_b32_e32 v18, v0
	v_mov_b32_e32 v19, v0
	v_mov_b32_e32 v20, v0
	v_mov_b32_e32 v21, v0
	v_mov_b32_e32 v22, v0
	v_mov_b32_e32 v23, v0
	v_mov_b32_e32 v32, v0
	v_mov_b32_e32 v33, v0
	v_mov_b32_e32 v34, v0
	v_mov_b32_e32 v35, v0
	v_mov_b32_e32 v36, v0
	v_mov_b32_e32 v37, v0
	v_mov_b32_e32 v38, v0
	v_mov_b32_e32 v39, v0
	v_mov_b32_e32 v48, v0
	v_mov_b32_e32 v49, v0
	v_mov_b32_e32 v50, v0
	v_mov_b32_e32 v51, v0
	v_mov_b32_e32 v52, v0
	v_mov_b32_e32 v53, v0
	v_mov_b32_e32 v54, v0
	v_mov_b32_e32 v55, v0
	v_mov_b32_e32 v8, v0
	v_mov_b32_e32 v9, v0
	v_mov_b32_e32 v10, v0
	v_mov_b32_e32 v11, v0
	v_mov_b32_e32 v12, v0
	v_mov_b32_e32 v13, v0
	v_mov_b32_e32 v14, v0
	v_mov_b32_e32 v15, v0
	v_mov_b32_e32 v24, v0
	v_mov_b32_e32 v25, v0
	v_mov_b32_e32 v26, v0
	v_mov_b32_e32 v27, v0
	v_mov_b32_e32 v28, v0
	v_mov_b32_e32 v29, v0
	v_mov_b32_e32 v30, v0
	v_mov_b32_e32 v31, v0
	v_mov_b32_e32 v40, v0
	v_mov_b32_e32 v41, v0
	v_mov_b32_e32 v42, v0
	v_mov_b32_e32 v43, v0
	v_mov_b32_e32 v44, v0
	v_mov_b32_e32 v45, v0
	v_mov_b32_e32 v46, v0
	v_mov_b32_e32 v47, v0
	v_mov_b32_e32 v56, v0
	v_mov_b32_e32 v57, v0
	v_mov_b32_e32 v58, v0
	v_mov_b32_e32 v59, v0
	v_mov_b32_e32 v60, v0
	v_mov_b32_e32 v61, v0
	v_mov_b32_e32 v62, v0
	v_mov_b32_e32 v63, v0
	v_mov_b32_e32 v64, v0
	v_mov_b32_e32 v65, v0
	v_mov_b32_e32 v66, v0
	v_mov_b32_e32 v67, v0
	v_mov_b32_e32 v68, v0
	v_mov_b32_e32 v69, v0
	v_mov_b32_e32 v70, v0
	v_mov_b32_e32 v71, v0
	v_mov_b32_e32 v98, v0
	v_mov_b32_e32 v99, v0
	v_mov_b32_e32 v100, v0
	v_mov_b32_e32 v101, v0
	v_mov_b32_e32 v102, v0
	v_mov_b32_e32 v103, v0
	v_mov_b32_e32 v104, v0
	v_mov_b32_e32 v105, v0
	v_mov_b32_e32 v114, v0
	v_mov_b32_e32 v115, v0
	v_mov_b32_e32 v116, v0
	v_mov_b32_e32 v117, v0
	v_mov_b32_e32 v118, v0
	v_mov_b32_e32 v119, v0
	v_mov_b32_e32 v120, v0
	v_mov_b32_e32 v121, v0
	v_mov_b32_e32 v130, v0
	v_mov_b32_e32 v131, v0
	v_mov_b32_e32 v132, v0
	v_mov_b32_e32 v133, v0
	v_mov_b32_e32 v134, v0
	v_mov_b32_e32 v135, v0
	v_mov_b32_e32 v136, v0
	v_mov_b32_e32 v137, v0
	v_mov_b32_e32 v80, v0
	v_mov_b32_e32 v81, v0
	v_mov_b32_e32 v82, v0
	v_mov_b32_e32 v83, v0
	v_mov_b32_e32 v92, v0
	v_mov_b32_e32 v93, v0
	v_mov_b32_e32 v94, v0
	v_mov_b32_e32 v95, v0
	v_mov_b32_e32 v106, v0
	v_mov_b32_e32 v107, v0
	v_mov_b32_e32 v108, v0
	v_mov_b32_e32 v109, v0
	v_mov_b32_e32 v110, v0
	v_mov_b32_e32 v111, v0
	v_mov_b32_e32 v112, v0
	v_mov_b32_e32 v113, v0
	v_mov_b32_e32 v122, v0
	v_mov_b32_e32 v123, v0
	v_mov_b32_e32 v124, v0
	v_mov_b32_e32 v125, v0
	v_mov_b32_e32 v126, v0
	v_mov_b32_e32 v127, v0
	v_mov_b32_e32 v128, v0
	v_mov_b32_e32 v129, v0
	v_mov_b32_e32 v138, v0
	v_mov_b32_e32 v139, v0
	v_mov_b32_e32 v140, v0
	v_mov_b32_e32 v141, v0
	v_mov_b32_e32 v142, v0
	v_mov_b32_e32 v143, v0
	v_mov_b32_e32 v144, v0
	v_mov_b32_e32 v145, v0
	.p2align 6

.LBB0_1495:
	v_mov_b64_e32 v[0:1], s[18:19]
	v_cmp_lt_i64_e32 vcc, s[10:11], v[0:1]
	s_lshl_b32 s22, s21, 20
	s_and_b64 s[10:11], vcc, exec
	s_cselect_b32 s48, s22, s50
	s_lshl_b32 s23, s20, 20
	s_and_b64 s[10:11], vcc, exec
	v_mov_b32_e32 v0, 0
	s_cselect_b32 s49, s23, s51
	s_add_i32 s50, s50, 0x80080
	s_addk_i32 s51, 0x100
	s_mov_b32 s52, -2
	v_mov_b32_e32 v1, v0
	v_mov_b32_e32 v2, v0
	v_mov_b32_e32 v3, v0
	v_mov_b32_e32 v4, v0
	v_mov_b32_e32 v5, v0
	v_mov_b32_e32 v6, v0
	v_mov_b32_e32 v7, v0
	v_mov_b32_e32 v12, v0
	v_mov_b32_e32 v13, v0
	v_mov_b32_e32 v14, v0
	v_mov_b32_e32 v15, v0
	s_waitcnt vmcnt(15)
	v_mov_b32_e32 v20, v0
	v_mov_b32_e32 v21, v0
	v_mov_b32_e32 v22, v0
	v_mov_b32_e32 v23, v0
	v_mov_b32_e32 v48, v0
	v_mov_b32_e32 v49, v0
	v_mov_b32_e32 v50, v0
	v_mov_b32_e32 v51, v0
	v_mov_b32_e32 v52, v0
	v_mov_b32_e32 v53, v0
	v_mov_b32_e32 v54, v0
	v_mov_b32_e32 v55, v0
	v_mov_b32_e32 v56, v0
	v_mov_b32_e32 v57, v0
	v_mov_b32_e32 v58, v0
	v_mov_b32_e32 v59, v0
	s_waitcnt vmcnt(14)
	v_mov_b32_e32 v60, v0
	v_mov_b32_e32 v61, v0
	v_mov_b32_e32 v62, v0
	v_mov_b32_e32 v63, v0
	v_mov_b32_e32 v8, v0
	v_mov_b32_e32 v9, v0
	v_mov_b32_e32 v10, v0
	v_mov_b32_e32 v11, v0
	v_mov_b32_e32 v16, v0
	v_mov_b32_e32 v17, v0
	v_mov_b32_e32 v18, v0
	v_mov_b32_e32 v19, v0
	v_mov_b32_e32 v24, v0
	v_mov_b32_e32 v25, v0
	v_mov_b32_e32 v26, v0
	v_mov_b32_e32 v27, v0
	v_mov_b32_e32 v28, v0
	v_mov_b32_e32 v29, v0
	v_mov_b32_e32 v30, v0
	v_mov_b32_e32 v31, v0
	v_mov_b32_e32 v64, v0
	v_mov_b32_e32 v65, v0
	v_mov_b32_e32 v66, v0
	v_mov_b32_e32 v67, v0
	v_mov_b32_e32 v68, v0
	v_mov_b32_e32 v69, v0
	v_mov_b32_e32 v70, v0
	v_mov_b32_e32 v71, v0
	v_mov_b32_e32 v72, v0
	v_mov_b32_e32 v73, v0
	v_mov_b32_e32 v74, v0
	v_mov_b32_e32 v75, v0
	v_mov_b32_e32 v76, v0
	v_mov_b32_e32 v77, v0
	v_mov_b32_e32 v78, v0
	v_mov_b32_e32 v79, v0
	v_mov_b32_e32 v80, v0
	v_mov_b32_e32 v81, v0
	v_mov_b32_e32 v82, v0
	v_mov_b32_e32 v83, v0
	v_mov_b32_e32 v84, v0
	v_mov_b32_e32 v85, v0
	v_mov_b32_e32 v86, v0
	v_mov_b32_e32 v87, v0
	v_mov_b32_e32 v88, v0
	v_mov_b32_e32 v89, v0
	v_mov_b32_e32 v90, v0
	v_mov_b32_e32 v91, v0
	v_mov_b32_e32 v92, v0
	v_mov_b32_e32 v93, v0
	v_mov_b32_e32 v94, v0
	v_mov_b32_e32 v95, v0
	v_mov_b32_e32 v114, v0
	v_mov_b32_e32 v115, v0
	v_mov_b32_e32 v116, v0
	v_mov_b32_e32 v117, v0
	v_mov_b32_e32 v118, v0
	v_mov_b32_e32 v119, v0
	v_mov_b32_e32 v120, v0
	v_mov_b32_e32 v121, v0
	v_mov_b32_e32 v122, v0
	v_mov_b32_e32 v123, v0
	v_mov_b32_e32 v124, v0
	v_mov_b32_e32 v125, v0
	v_mov_b32_e32 v126, v0
	v_mov_b32_e32 v127, v0
	v_mov_b32_e32 v128, v0
	v_mov_b32_e32 v129, v0
	v_mov_b32_e32 v98, v0
	v_mov_b32_e32 v99, v0
	v_mov_b32_e32 v100, v0
	v_mov_b32_e32 v101, v0
	v_mov_b32_e32 v102, v0
	v_mov_b32_e32 v103, v0
	v_mov_b32_e32 v104, v0
	v_mov_b32_e32 v105, v0
	v_mov_b32_e32 v106, v0
	v_mov_b32_e32 v107, v0
	v_mov_b32_e32 v108, v0
	v_mov_b32_e32 v109, v0
	v_mov_b32_e32 v110, v0
	v_mov_b32_e32 v111, v0
	v_mov_b32_e32 v112, v0
	v_mov_b32_e32 v113, v0
	v_mov_b32_e32 v130, v0
	v_mov_b32_e32 v131, v0
	v_mov_b32_e32 v132, v0
	v_mov_b32_e32 v133, v0
	v_mov_b32_e32 v134, v0
	v_mov_b32_e32 v135, v0
	v_mov_b32_e32 v136, v0
	v_mov_b32_e32 v137, v0
	v_mov_b32_e32 v138, v0
	v_mov_b32_e32 v139, v0
	v_mov_b32_e32 v140, v0
	v_mov_b32_e32 v141, v0
	v_mov_b32_e32 v142, v0
	v_mov_b32_e32 v143, v0
	v_mov_b32_e32 v144, v0
	v_mov_b32_e32 v145, v0
	.p2align 6

.LBB0_1513:
	v_mov_b64_e32 v[0:1], s[18:19]
	v_cmp_lt_i64_e32 vcc, s[10:11], v[0:1]
	s_lshl_b32 s16, s15, 20
	s_and_b64 s[10:11], vcc, exec
	s_cselect_b32 s47, s16, s49
	s_lshl_b32 s17, s14, 20
	s_and_b64 s[10:11], vcc, exec
	v_mov_b32_e32 v0, 0
	s_cselect_b32 s48, s17, s50
	s_add_i32 s49, s49, 0x80080
	s_addk_i32 s50, 0x100
	s_mov_b32 s51, -2
	v_mov_b32_e32 v1, v0
	v_mov_b32_e32 v2, v0
	v_mov_b32_e32 v3, v0
	v_mov_b32_e32 v4, v0
	v_mov_b32_e32 v5, v0
	v_mov_b32_e32 v6, v0
	v_mov_b32_e32 v7, v0
	v_mov_b32_e32 v8, v0
	v_mov_b32_e32 v9, v0
	v_mov_b32_e32 v10, v0
	v_mov_b32_e32 v11, v0
	v_mov_b32_e32 v12, v0
	v_mov_b32_e32 v13, v0
	v_mov_b32_e32 v14, v0
	v_mov_b32_e32 v15, v0
	v_mov_b32_e32 v32, v0
	v_mov_b32_e32 v33, v0
	v_mov_b32_e32 v34, v0
	v_mov_b32_e32 v35, v0
	v_mov_b32_e32 v36, v0
	v_mov_b32_e32 v37, v0
	v_mov_b32_e32 v38, v0
	v_mov_b32_e32 v39, v0
	v_mov_b32_e32 v40, v0
	v_mov_b32_e32 v41, v0
	v_mov_b32_e32 v42, v0
	v_mov_b32_e32 v43, v0
	v_mov_b32_e32 v44, v0
	v_mov_b32_e32 v45, v0
	v_mov_b32_e32 v46, v0
	v_mov_b32_e32 v47, v0
	s_waitcnt vmcnt(14)
	v_mov_b32_e32 v16, v0
	v_mov_b32_e32 v17, v0
	v_mov_b32_e32 v18, v0
	v_mov_b32_e32 v19, v0
	v_mov_b32_e32 v20, v0
	v_mov_b32_e32 v21, v0
	v_mov_b32_e32 v22, v0
	v_mov_b32_e32 v23, v0
	v_mov_b32_e32 v24, v0
	v_mov_b32_e32 v25, v0
	v_mov_b32_e32 v26, v0
	v_mov_b32_e32 v27, v0
	v_mov_b32_e32 v28, v0
	v_mov_b32_e32 v29, v0
	v_mov_b32_e32 v30, v0
	v_mov_b32_e32 v31, v0
	v_mov_b32_e32 v48, v0
	v_mov_b32_e32 v49, v0
	v_mov_b32_e32 v50, v0
	v_mov_b32_e32 v51, v0
	v_mov_b32_e32 v52, v0
	v_mov_b32_e32 v53, v0
	v_mov_b32_e32 v54, v0
	v_mov_b32_e32 v55, v0
	v_mov_b32_e32 v56, v0
	v_mov_b32_e32 v57, v0
	v_mov_b32_e32 v58, v0
	v_mov_b32_e32 v59, v0
	v_mov_b32_e32 v60, v0
	v_mov_b32_e32 v61, v0
	v_mov_b32_e32 v62, v0
	v_mov_b32_e32 v63, v0
	v_mov_b32_e32 v80, v0
	v_mov_b32_e32 v81, v0
	v_mov_b32_e32 v82, v0
	v_mov_b32_e32 v83, v0
	v_mov_b32_e32 v84, v0
	v_mov_b32_e32 v85, v0
	v_mov_b32_e32 v86, v0
	v_mov_b32_e32 v87, v0
	v_mov_b32_e32 v88, v0
	v_mov_b32_e32 v89, v0
	v_mov_b32_e32 v90, v0
	v_mov_b32_e32 v91, v0
	v_mov_b32_e32 v92, v0
	v_mov_b32_e32 v93, v0
	v_mov_b32_e32 v94, v0
	v_mov_b32_e32 v95, v0
	v_mov_b32_e32 v114, v0
	v_mov_b32_e32 v115, v0
	v_mov_b32_e32 v116, v0
	v_mov_b32_e32 v117, v0
	v_mov_b32_e32 v118, v0
	v_mov_b32_e32 v119, v0
	v_mov_b32_e32 v120, v0
	v_mov_b32_e32 v121, v0
	v_mov_b32_e32 v122, v0
	v_mov_b32_e32 v123, v0
	v_mov_b32_e32 v124, v0
	v_mov_b32_e32 v125, v0
	v_mov_b32_e32 v126, v0
	v_mov_b32_e32 v127, v0
	v_mov_b32_e32 v128, v0
	v_mov_b32_e32 v129, v0
	v_mov_b32_e32 v98, v0
	v_mov_b32_e32 v99, v0
	v_mov_b32_e32 v100, v0
	v_mov_b32_e32 v101, v0
	v_mov_b32_e32 v102, v0
	v_mov_b32_e32 v103, v0
	v_mov_b32_e32 v104, v0
	v_mov_b32_e32 v105, v0
	v_mov_b32_e32 v106, v0
	v_mov_b32_e32 v107, v0
	v_mov_b32_e32 v108, v0
	v_mov_b32_e32 v109, v0
	v_mov_b32_e32 v110, v0
	v_mov_b32_e32 v111, v0
	v_mov_b32_e32 v112, v0
	v_mov_b32_e32 v113, v0
	v_mov_b32_e32 v130, v0
	v_mov_b32_e32 v131, v0
	v_mov_b32_e32 v132, v0
	v_mov_b32_e32 v133, v0
	v_mov_b32_e32 v134, v0
	v_mov_b32_e32 v135, v0
	v_mov_b32_e32 v136, v0
	v_mov_b32_e32 v137, v0
	v_mov_b32_e32 v138, v0
	v_mov_b32_e32 v139, v0
	v_mov_b32_e32 v140, v0
	v_mov_b32_e32 v141, v0
	v_mov_b32_e32 v142, v0
	v_mov_b32_e32 v143, v0
	v_mov_b32_e32 v144, v0
	v_mov_b32_e32 v145, v0
	.p2align 6

.LBB0_1638:
	v_mov_b64_e32 v[0:1], s[6:7]
	v_cmp_lt_i64_e32 vcc, s[10:11], v[0:1]
	s_lshl_b32 s16, s15, 20
	s_and_b64 s[10:11], vcc, exec
	s_cselect_b32 s39, s16, s41
	s_lshl_b32 s17, s14, 20
	s_and_b64 s[10:11], vcc, exec
	v_mov_b32_e32 v0, 0
	s_cselect_b32 s40, s17, s42
	s_add_i32 s41, s41, 0x80080
	s_addk_i32 s42, 0x100
	s_mov_b32 s43, -2
	v_mov_b32_e32 v1, v0
	v_mov_b32_e32 v2, v0
	v_mov_b32_e32 v3, v0
	v_mov_b32_e32 v12, v0
	v_mov_b32_e32 v13, v0
	v_mov_b32_e32 v14, v0
	v_mov_b32_e32 v15, v0
	v_mov_b32_e32 v4, v0
	v_mov_b32_e32 v5, v0
	v_mov_b32_e32 v6, v0
	v_mov_b32_e32 v7, v0
	v_mov_b32_e32 v20, v0
	v_mov_b32_e32 v21, v0
	v_mov_b32_e32 v22, v0
	v_mov_b32_e32 v23, v0
	v_mov_b32_e32 v8, v0
	v_mov_b32_e32 v9, v0
	v_mov_b32_e32 v10, v0
	v_mov_b32_e32 v11, v0
	v_mov_b32_e32 v24, v0
	v_mov_b32_e32 v25, v0
	v_mov_b32_e32 v26, v0
	v_mov_b32_e32 v27, v0
	v_mov_b32_e32 v16, v0
	v_mov_b32_e32 v17, v0
	v_mov_b32_e32 v18, v0
	v_mov_b32_e32 v19, v0
	v_mov_b32_e32 v28, v0
	v_mov_b32_e32 v29, v0
	v_mov_b32_e32 v30, v0
	v_mov_b32_e32 v31, v0
	v_mov_b32_e32 v36, v0
	v_mov_b32_e32 v37, v0
	v_mov_b32_e32 v38, v0
	v_mov_b32_e32 v39, v0
	v_mov_b32_e32 v52, v0
	v_mov_b32_e32 v53, v0
	v_mov_b32_e32 v54, v0
	v_mov_b32_e32 v55, v0
	v_mov_b32_e32 v44, v0
	v_mov_b32_e32 v45, v0
	v_mov_b32_e32 v46, v0
	v_mov_b32_e32 v47, v0
	v_mov_b32_e32 v68, v0
	v_mov_b32_e32 v69, v0
	v_mov_b32_e32 v70, v0
	v_mov_b32_e32 v71, v0
	v_mov_b32_e32 v56, v0
	v_mov_b32_e32 v57, v0
	v_mov_b32_e32 v58, v0
	v_mov_b32_e32 v59, v0
	v_mov_b32_e32 v80, v0
	v_mov_b32_e32 v81, v0
	v_mov_b32_e32 v82, v0
	v_mov_b32_e32 v83, v0
	v_mov_b32_e32 v72, v0
	v_mov_b32_e32 v73, v0
	v_mov_b32_e32 v74, v0
	v_mov_b32_e32 v75, v0
	v_mov_b32_e32 v88, v0
	v_mov_b32_e32 v89, v0
	v_mov_b32_e32 v90, v0
	v_mov_b32_e32 v91, v0
	v_mov_b32_e32 v32, v0
	v_mov_b32_e32 v33, v0
	v_mov_b32_e32 v34, v0
	v_mov_b32_e32 v35, v0
	v_mov_b32_e32 v60, v0
	v_mov_b32_e32 v61, v0
	v_mov_b32_e32 v62, v0
	v_mov_b32_e32 v63, v0
	v_mov_b32_e32 v40, v0
	v_mov_b32_e32 v41, v0
	v_mov_b32_e32 v42, v0
	v_mov_b32_e32 v43, v0
	v_mov_b32_e32 v76, v0
	v_mov_b32_e32 v77, v0
	v_mov_b32_e32 v78, v0
	v_mov_b32_e32 v79, v0
	v_mov_b32_e32 v48, v0
	v_mov_b32_e32 v49, v0
	v_mov_b32_e32 v50, v0
	v_mov_b32_e32 v51, v0
	v_mov_b32_e32 v84, v0
	v_mov_b32_e32 v85, v0
	v_mov_b32_e32 v86, v0
	v_mov_b32_e32 v87, v0
	v_mov_b32_e32 v64, v0
	v_mov_b32_e32 v65, v0
	v_mov_b32_e32 v66, v0
	v_mov_b32_e32 v67, v0
	v_mov_b32_e32 v92, v0
	v_mov_b32_e32 v93, v0
	v_mov_b32_e32 v94, v0
	v_mov_b32_e32 v95, v0
	v_mov_b32_e32 v98, v0
	v_mov_b32_e32 v99, v0
	v_mov_b32_e32 v100, v0
	v_mov_b32_e32 v101, v0
	v_mov_b32_e32 v110, v0
	v_mov_b32_e32 v111, v0
	v_mov_b32_e32 v112, v0
	v_mov_b32_e32 v113, v0
	v_mov_b32_e32 v102, v0
	v_mov_b32_e32 v103, v0
	v_mov_b32_e32 v104, v0
	v_mov_b32_e32 v105, v0
	v_mov_b32_e32 v118, v0
	v_mov_b32_e32 v119, v0
	v_mov_b32_e32 v120, v0
	v_mov_b32_e32 v121, v0
	v_mov_b32_e32 v106, v0
	v_mov_b32_e32 v107, v0
	v_mov_b32_e32 v108, v0
	v_mov_b32_e32 v109, v0
	v_mov_b32_e32 v122, v0
	v_mov_b32_e32 v123, v0
	v_mov_b32_e32 v124, v0
	v_mov_b32_e32 v125, v0
	v_mov_b32_e32 v114, v0
	v_mov_b32_e32 v115, v0
	v_mov_b32_e32 v116, v0
	v_mov_b32_e32 v117, v0
	v_mov_b32_e32 v126, v0
	v_mov_b32_e32 v127, v0
	v_mov_b32_e32 v128, v0
	v_mov_b32_e32 v129, v0
	.p2align 6

.LBB0_1700:
	s_getreg_b32 s2, hwreg(HW_REG_HW_ID, 0, 6)
	s_and_b32 s2, s2, 63
	s_lshl_b32 s2, s2, 2
	s_add_i32 s2, s2, 0
	s_add_i32 s2, s2, 0x20010
	v_mov_b32_e32 v4, s2
	ds_read_b32 v37, v4
	v_ashrrev_i32_e32 v4, 3, v44
	v_add_u32_e32 v4, v4, v45
	v_ashrrev_i32_e32 v5, 31, v4
	v_mbcnt_lo_u32_b32 v36, -1, 0
	v_mbcnt_hi_u32_b32 v36, -1, v36
	v_lshlrev_b64 v[4:5], 16, v[4:5]
	v_and_b32_e32 v46, 63, v36
	v_lshl_or_b32 v4, v46, 2, v4
	v_lshl_add_u64 v[4:5], s[6:7], 0, v[4:5]
	s_mov_b32 s2, -16
	s_mov_b32 s10, 0
	v_add_co_u32_e32 v134, vcc, 0xffff8000, v4
	s_nop 1
	v_addc_co_u32_e32 v135, vcc, -1, v5, vcc
	global_load_dword v100, v[134:135], off offset:-3840
	global_load_dword v101, v[4:5], off offset:-3840
	global_load_dword v102, v[134:135], off offset:-3584
	global_load_dword v103, v[4:5], off offset:-3584
	global_load_dword v104, v[134:135], off offset:-3328
	global_load_dword v105, v[4:5], off offset:-3328
	global_load_dword v106, v[134:135], off offset:-3072
	global_load_dword v107, v[4:5], off offset:-3072
	global_load_dword v108, v[134:135], off offset:-2816
	global_load_dword v109, v[4:5], off offset:-2816
	global_load_dword v110, v[134:135], off offset:-2560
	global_load_dword v111, v[4:5], off offset:-2560
	global_load_dword v112, v[134:135], off offset:-2304
	global_load_dword v113, v[4:5], off offset:-2304
	global_load_dword v114, v[134:135], off offset:-2048
	global_load_dword v115, v[4:5], off offset:-2048
	global_load_dword v116, v[134:135], off offset:-1792
	global_load_dword v117, v[4:5], off offset:-1792
	global_load_dword v118, v[134:135], off offset:-1536
	global_load_dword v119, v[4:5], off offset:-1536
	global_load_dword v120, v[134:135], off offset:-1280
	global_load_dword v121, v[4:5], off offset:-1280
	global_load_dword v122, v[134:135], off offset:-1024
	global_load_dword v123, v[4:5], off offset:-1024
	global_load_dword v124, v[134:135], off offset:-768
	global_load_dword v125, v[4:5], off offset:-768
	global_load_dword v126, v[134:135], off offset:-512
	global_load_dword v127, v[4:5], off offset:-512
	global_load_dword v128, v[134:135], off offset:-256
	global_load_dword v129, v[4:5], off offset:-256
	global_load_dword v130, v[134:135], off
	global_load_dword v131, v[4:5], off
	.p2align 6

.LBB0_1761:
	s_or_b64 exec, exec, s[38:39]
	v_cmp_le_i32_e32 vcc, s0, v158
	s_or_b64 s[36:37], vcc, s[36:37]
	v_add_u32_e32 v157, s79, v157
	s_andn2_b64 exec, exec, s[36:37]
	s_cbranch_execz .LBB0_1758
	.p2align 6
